# expert-weight conversion rider moved from the GQA attention units (HBM-bound) into the differential-attention units; dead zero-init v_mov before fp8 pack pairs replaced by s_nop
# speedup vs baseline: 1.0028x; 1.0008x over previous
; DI void attn_unit_a8(unsigned char* lds, const AttnArgs& a) {
;     ...
;     const int wn4 = (tid & 63) * 4;
;     constexpr int WPITCH = 36;
;     auto w_decode = [&](int j, const float*& src, unsigned char*& dst, int& ld, int& n0, int& k0, bool& gu) __attribute__((always_inline)) {
;         const int g = (j >> 2) * 512 + a.wl, e = g / 96, rr = g - e * 96; KParamsPtr kp = kparams();
;         if (rr < 64) { src = kp->w_gu + ((size_t)a.wli * NE + e) * (1024 * 2048); dst = kp->ws + WS_WGU + (size_t)a.wli * SZ_WGU + (size_t)e * 2048 * 1024; ld = 2048; n0 = (rr & 7) * 256; k0 = ((rr >> 3) * 4 + (j & 3)) * 32; gu = true; }
;         else { const int q = rr - 64; src = kp->w_dn + ((size_t)a.wli * NE + e) * (1024 * 1024); dst = kp->ws + WS_WDN + (size_t)a.wli * SZ_WDN + (size_t)e * 1024 * 1024; ld = 1024; n0 = (q & 3) * 256; k0 = ((q >> 2) * 4 + (j & 3)) * 32; gu = false; } };
;     auto w_issue = [&](int j) __attribute__((always_inline)) { const float* src; unsigned char* dst; int ld, n0, k0; bool gu; w_decode(j, src, dst, ld, n0, k0, gu);
;         const float* p = src + (size_t)(k0 + 4 * wid) * ld + n0 + wn4;
;         wq[0] = __builtin_nontemporal_load((const f32x4*)p); wq[1] = __builtin_nontemporal_load((const f32x4*)(p + ld));
;         wq[2] = __builtin_nontemporal_load((const f32x4*)(p + (size_t)2 * ld)); wq[3] = __builtin_nontemporal_load((const f32x4*)(p + (size_t)3 * ld)); };
;     auto w_cvt = [&]() __attribute__((always_inline)) { unsigned char* t8 = lds + AT_WT + wn4 * WPITCH + 4 * wid;
; #pragma unroll
;         for (int j = 0; j < 4; ++j) *(unsigned*)(t8 + j * WPITCH) = pk4_fp8_mul64(wq[0][j], wq[1][j], wq[2][j], wq[3][j]); };
;     const int wcol = tid >> 1, whalf = tid & 1;
;     const unsigned wper_gu = (unsigned)((wcol >> 7) * 256 + (wcol & 96) + invperm32(wcol & 31)) * 1024u + 16u * whalf;
;     const unsigned wper_dn = (unsigned)fwd_lane16(wcol) * 1024u + 16u * whalf;
; template <int li>
; DI void layer_phases(unsigned char* smem, LAS unsigned char* ldsL, const int lo, const int hi) {
;     ...
;               const float lam_init = 0.8f - 0.6f * __expf(-0.3f * (float)li);
;               float lam;
;               { const float* dl = kp->d_lambda + li * 128; float a = 0.f, b = 0.f; if (lane < 32) { a = dl[lane] * dl[32 + lane]; b = dl[64 + lane] * dl[96 + lane]; }
;                 lam = __expf(wave_sum(a)) - __expf(wave_sum(b)) + lam_init; }
.LBB0_654:
	s_or_b64 exec, exec, s[6:7]
	v_mbcnt_lo_u32_b32 v1, -1, 0
	v_mbcnt_hi_u32_b32 v5, -1, v1
	v_and_b32_e32 v1, 64, v5
	v_add_u32_e32 v6, 64, v1
	v_xor_b32_e32 v1, 32, v5
	v_cmp_lt_i32_e32 vcc, v1, v6
	v_xor_b32_e32 v7, 16, v5
	s_and_b32 s6, 0xffff, s9
	v_cndmask_b32_e32 v1, v5, v1, vcc
	v_lshlrev_b32_e32 v1, 2, v1
	ds_bpermute_b32 v4, v1, v3
	v_cmp_lt_i32_e32 vcc, v7, v6
	ds_bpermute_b32 v8, v1, v2
	s_cmp_lg_u32 s6, 0
	s_cselect_b64 s[6:7], -1, 0
	s_waitcnt lgkmcnt(1)
	v_add_f32_e32 v3, v3, v4
	v_cndmask_b32_e32 v4, v5, v7, vcc
	v_lshlrev_b32_e32 v206, 2, v4
	ds_bpermute_b32 v4, v206, v3
	v_xor_b32_e32 v7, 8, v5
	v_cmp_lt_i32_e32 vcc, v7, v6
	s_waitcnt lgkmcnt(1)
	v_add_f32_e32 v2, v2, v8
	s_cmp_lg_u64 s[6:7], 0
	s_waitcnt lgkmcnt(0)
	v_add_f32_e32 v3, v3, v4
	v_cndmask_b32_e32 v4, v5, v7, vcc
	v_lshlrev_b32_e32 v207, 2, v4
	ds_bpermute_b32 v4, v207, v3
	v_xor_b32_e32 v7, 4, v5
	v_cmp_lt_i32_e32 vcc, v7, v6
	s_addc_u32 s64, s8, 0
	s_cmpk_gt_i32 s2, 0x21f
	s_waitcnt lgkmcnt(0)
	v_add_f32_e32 v3, v3, v4
	v_cndmask_b32_e32 v4, v5, v7, vcc
	ds_bpermute_b32 v7, v206, v2
	v_lshlrev_b32_e32 v208, 2, v4
	ds_bpermute_b32 v4, v208, v3
	s_mov_b32 s7, 0
	s_waitcnt lgkmcnt(1)
	v_add_f32_e32 v2, v2, v7
	ds_bpermute_b32 v7, v207, v2
	s_waitcnt lgkmcnt(1)
	v_add_f32_e32 v3, v3, v4
	v_xor_b32_e32 v4, 2, v5
	v_cmp_lt_i32_e32 vcc, v4, v6
	s_waitcnt lgkmcnt(0)
	v_add_f32_e32 v2, v2, v7
	ds_bpermute_b32 v7, v208, v2
	v_cndmask_b32_e32 v4, v5, v4, vcc
	v_lshlrev_b32_e32 v209, 2, v4
	ds_bpermute_b32 v4, v209, v3
	s_waitcnt lgkmcnt(1)
	v_add_f32_e32 v2, v2, v7
	ds_bpermute_b32 v7, v209, v2
	s_waitcnt lgkmcnt(1)
	v_add_f32_e32 v4, v3, v4
	v_xor_b32_e32 v3, 1, v5
	v_cmp_lt_i32_e32 vcc, v3, v6
	s_waitcnt lgkmcnt(0)
	v_add_f32_e32 v2, v2, v7
	v_cndmask_b32_e32 v3, v5, v3, vcc
	v_lshlrev_b32_e32 v210, 2, v3
	ds_bpermute_b32 v5, v210, v4
	ds_bpermute_b32 v3, v210, v2
	s_cbranch_scc1 .LBB0_665
	s_load_dwordx2 s[8:9], s[10:11], 0xd8
	s_waitcnt lgkmcnt(0)
	v_add_f32_e32 v4, v4, v5
	v_add_f32_e32 v2, v2, v3
	v_mul_f32_e32 v4, 0x3fb8aa3b, v4
	v_mul_f32_e32 v2, 0x3fb8aa3b, v2
	v_exp_f32_e32 v4, v4
	v_exp_f32_e32 v2, v2
	s_add_u32 s22, s8, 0x25054000
	s_load_dwordx2 s[10:11], s[10:11], 0x90
	s_addc_u32 s23, s9, 0
	s_add_u32 s24, s8, 0x26154000
	s_addc_u32 s25, s9, 0
	v_sub_f32_e32 v2, v4, v2
	s_add_u32 s28, s8, 0x27ad4000
	v_add_f32_e32 v2, 0x3e4ccccc, v2
	s_addc_u32 s29, s9, 0
	s_mov_b32 s36, 0x41800000
	v_mul_f32_e32 v211, 0x41800000, v2
	s_movk_i32 s37, 0x1100
	v_mov_b32_e32 v179, 0
	s_movk_i32 s38, 0x50
	v_mov_b32_e32 v212, 0x358637bd
	s_mov_b32 s39, 0x800000
	s_mov_b64 s[12:13], 0x2add4300
	s_mov_b32 s40, 0xc3e00000
	s_mov_b32 s41, 0x2add4000
	v_mov_b32_e32 v213, 0x43e00000
	s_mov_b32 s42, s2
	s_load_dwordx2 s[66:67], s[0:1], 0xb0
	s_load_dwordx2 s[68:69], s[0:1], 0xc0
	s_load_dwordx2 s[70:71], s[0:1], 0xd8
	s_mov_b32 s62, 0x3c800000
	v_lshrrev_b32_e32 v236, 6, v0
	v_and_b32_e32 v237, 63, v0
	v_lshlrev_b32_e32 v235, 4, v237
	v_mul_u32_u24_e32 v238, 0x90, v237
	v_lshl_add_u32 v252, v236, 2, v238
	v_add_u32_e32 v252, 0x14000, v252
	v_lshrrev_b32_e32 v239, 1, v0
	v_and_b32_e32 v240, 1, v0
	v_mul_u32_u24_e32 v253, 36, v239
	v_lshl_add_u32 v253, v240, 4, v253
	v_add_u32_e32 v253, 0x10000, v253
	v_and_b32_e32 v241, 0x80, v239
	v_lshlrev_b32_e32 v241, 1, v241
	v_and_b32_e32 v242, 0x60, v239
	v_bfe_u32 v243, v239, 2, 1
	v_bfe_u32 v244, v239, 3, 2
	v_and_b32_e32 v245, 3, v239
	v_lshl_or_b32 v245, v243, 4, v245
	v_lshl_or_b32 v245, v244, 2, v245
	v_add3_u32 v241, v241, v242, v245
	v_lshlrev_b32_e32 v254, 10, v241
	v_lshl_or_b32 v254, v240, 4, v254
	v_bfe_u32 v241, v239, 3, 1
	v_bfe_u32 v242, v239, 6, 2
	v_bfe_u32 v243, v239, 2, 1
	v_bfe_u32 v244, v239, 4, 2
	v_and_b32_e32 v245, 3, v239
	v_lshl_or_b32 v245, v244, 2, v245
	v_lshl_or_b32 v245, v243, 4, v245
	v_lshl_or_b32 v245, v242, 5, v245
	v_lshl_or_b32 v245, v241, 7, v245
	v_lshlrev_b32_e32 v255, 10, v245
	v_lshl_or_b32 v255, v240, 4, v255
	s_nop 0
	v_readfirstlane_b32 s63, v236
	s_waitcnt lgkmcnt(0)

; DI f32x16 mfma8(v8i a, v8i b, f32x16 c) { return __builtin_amdgcn_mfma_scale_f32_32x32x64_f8f6f4(a, b, c, 0, 0, 0, 0, 0, 0); }
; DI void attn_unit_d8(unsigned char* lds, const AttnArgs& a) {
;     ...
;     qk(lds, 0, s0a, s0b);
;     if (wid >= 4) __builtin_amdgcn_s_setprio(1);
;     int sb = 0;
;     const v8i zz8 = (v8i){0, 0, 0, 0, 0, 0, 0, 0};
;     v8i PaX = zz8, PbX = zz8, PaY = zz8, PbY = zz8, vX0 = zz8, vX1 = zz8, vY0 = zz8, vY1 = zz8;
;     auto tile = [&](const unsigned char* Kb, const unsigned char* Kn, v8i& Pa, v8i& Pb, v8i& v0, v8i& v1, const v8i& Qa, const v8i& Qb, const v8i& w0, const v8i& w1) __attribute__((always_inline)) {
;         qk(Kb, 1, s1a, s1b);
;         v0 = rd32(Kb + voff); v1 = rd32(Kb + voff + 32 * A8_PITCH);
;         o0[0] = mfma8(w0, Qa, o0[0]); o1[0] = mfma8(w0, Qb, o1[0]); o0[1] = mfma8(w1, Qa, o0[1]); o1[1] = mfma8(w1, Qb, o1[1]);
;         expsum(s0a, l0); expsum(s0b, l1); pack4(s0a, Pa, 0); pack4(s0b, Pb, 0);
;         qk(Kn, 0, s0a, s0b);
;         expsum(s1a, l0); expsum(s1b, l1); pack4(s1a, Pa, 4); pack4(s1b, Pb, 4);
; #pragma unroll
;         for (int i = 0; i < 8; ++i) { __builtin_amdgcn_sched_group_barrier(0x008, 1, 0); __builtin_amdgcn_sched_group_barrier(0x402, 22, 0); }
;     };
;     for (int t = a.t0; t < a.t1; t += 2) {
;         const int s1 = sb + 1 >= 5 ? sb - 4 : sb + 1, s2 = sb + 2 >= 5 ? sb - 3 : sb + 2, s3 = sb + 3 >= 5 ? sb - 2 : sb + 3, s4 = sb + 4 >= 5 ? sb - 1 : sb + 4;
;         { const int ta = t + 3, tb = t + 4; gload(ta < a.t1 ? ta : a.t1 - 1, kreg0, vreg0); gload(tb < a.t1 ? tb : a.t1 - 1, kreg1, vreg1); }
;         tile(lds + sb * D8_SLOT, lds + s1 * D8_SLOT, PaX, PbX, vX0, vX1, PaY, PbY, vY0, vY1);
;         tile(lds + s1 * D8_SLOT, lds + s2 * D8_SLOT, PaY, PbY, vY0, vY1, PaX, PbX, vX0, vX1);
.LBB0_662:
	s_mov_b32 s61, 0
	v_mov_b32_e32 v2, 0
	s_mov_b32 s16, 0
	v_mov_b32_e32 v138, 0
	v_mov_b32_e32 v139, 0
	v_mov_b32_e32 v140, 0
	v_mov_b32_e32 v141, 0
	v_mov_b32_e32 v142, 0
	v_mov_b32_e32 v143, 0
	v_mov_b32_e32 v144, 0
	v_mov_b32_e32 v145, 0
	v_mov_b32_e32 v130, 0
	v_mov_b32_e32 v131, 0
	v_mov_b32_e32 v132, 0
	v_mov_b32_e32 v133, 0
	v_mov_b32_e32 v134, 0
	v_mov_b32_e32 v135, 0
	v_mov_b32_e32 v136, 0
	v_mov_b32_e32 v137, 0
	v_mov_b32_e32 v154, 0
	v_mov_b32_e32 v155, 0
	v_mov_b32_e32 v156, 0
	v_mov_b32_e32 v157, 0
	v_mov_b32_e32 v158, 0
	v_mov_b32_e32 v159, 0
	v_mov_b32_e32 v160, 0
	v_mov_b32_e32 v161, 0
	v_mov_b32_e32 v146, 0
	v_mov_b32_e32 v147, 0
	v_mov_b32_e32 v148, 0
	v_mov_b32_e32 v149, 0
	v_mov_b32_e32 v150, 0
	v_mov_b32_e32 v151, 0
	v_mov_b32_e32 v152, 0
	v_mov_b32_e32 v153, 0
	v_mov_b32_e32 v3, v2
	v_mov_b32_e32 v4, v2
	v_mov_b32_e32 v5, v2
	v_mov_b32_e32 v6, v2
	v_mov_b32_e32 v7, v2
	v_mov_b32_e32 v8, v2
	v_mov_b32_e32 v9, v2
	v_mov_b32_e32 v10, v2
	v_mov_b32_e32 v11, v2
	v_mov_b32_e32 v12, v2
	v_mov_b32_e32 v13, v2
	v_mov_b32_e32 v14, v2
	v_mov_b32_e32 v15, v2
	v_mov_b32_e32 v16, v2
	v_mov_b32_e32 v17, v2
	v_mov_b32_e32 v18, v2
	v_mov_b32_e32 v19, v2
	v_mov_b32_e32 v20, v2
	v_mov_b32_e32 v21, v2
	v_mov_b32_e32 v22, v2
	v_mov_b32_e32 v23, v2
	v_mov_b32_e32 v24, v2
	v_mov_b32_e32 v25, v2
	v_mov_b32_e32 v26, v2
	v_mov_b32_e32 v27, v2
	v_mov_b32_e32 v28, v2
	v_mov_b32_e32 v29, v2
	v_mov_b32_e32 v30, v2
	v_mov_b32_e32 v31, v2
	v_mov_b32_e32 v32, v2
	v_mov_b32_e32 v33, v2
	v_mov_b32_e32 v50, v2
	v_mov_b32_e32 v51, v2
	v_mov_b32_e32 v52, v2
	v_mov_b32_e32 v53, v2
	v_mov_b32_e32 v54, v2
	v_mov_b32_e32 v55, v2
	v_mov_b32_e32 v56, v2
	v_mov_b32_e32 v57, v2
	v_mov_b32_e32 v58, v2
	v_mov_b32_e32 v59, v2
	v_mov_b32_e32 v60, v2
	v_mov_b32_e32 v61, v2
	v_mov_b32_e32 v62, v2
	v_mov_b32_e32 v63, v2
	v_mov_b32_e32 v64, v2
	v_mov_b32_e32 v65, v2
	v_mov_b32_e32 v34, v2
	v_mov_b32_e32 v35, v2
	v_mov_b32_e32 v36, v2
	v_mov_b32_e32 v37, v2
	v_mov_b32_e32 v38, v2
	v_mov_b32_e32 v39, v2
	v_mov_b32_e32 v40, v2
	v_mov_b32_e32 v41, v2
	v_mov_b32_e32 v42, v2
	v_mov_b32_e32 v43, v2
	v_mov_b32_e32 v44, v2
	v_mov_b32_e32 v45, v2
	v_mov_b32_e32 v46, v2
	v_mov_b32_e32 v47, v2
	v_mov_b32_e32 v48, v2
	v_mov_b32_e32 v49, v2
	v_mov_b32_e32 v186, v2
	v_mov_b32_e32 v187, v2
	v_mov_b32_e32 v184, v2
	v_mov_b32_e32 v185, v2
	v_mov_b32_e32 v190, v2
	v_mov_b32_e32 v191, v2
	v_mov_b32_e32 v188, v2
	v_mov_b32_e32 v189, v2
.LBB0_663:
	s_cmp_gt_i32 s16, 3
	s_cselect_b32 s17, -4, 1
	s_add_i32 s18, s17, s16
	s_mul_i32 s6, s16, 0x2800
	s_cmp_gt_i32 s16, 2
	v_mfma_f32_32x32x64_f8f6f4 v[50:65], v[154:161], v[138:145], v[50:65]
	v_exp_f32_e32 v192, v90
	v_add_u32_e32 v90, s6, v218
	s_cselect_b32 s6, -3, 2
	s_add_i32 s6, s6, s16
	s_cmp_gt_i32 s16, 1
	s_cselect_b32 s19, -2, 3
	s_add_i32 s19, s19, s16
	s_cmp_gt_i32 s16, 0
	s_cselect_b32 s49, -1, 4
	s_min_u32 s54, s46, 64
	s_add_i32 s49, s49, s16
	s_cmp_lt_u32 s46, 61
	s_mul_i32 s17, s6, 0x2800
	s_mov_b32 s16, s6
	s_cselect_b64 s[52:53], -1, 0
	s_lshl_b32 s6, s54, 6
	s_add_i32 s54, s6, 0xc0
	s_add_i32 s55, s6, 0xfffff0c0
	s_and_b64 s[52:53], s[52:53], exec
	v_lshl_add_u64 v[98:99], v[182:183], 0, s[6:7]
	s_cselect_b32 s6, s54, s55
	s_cselect_b32 s53, s21, s48
	s_cselect_b32 s52, s20, s47
	s_min_u32 s56, s46, 63
	v_exp_f32_e32 v198, v82
	v_exp_f32_e32 v199, v83
	v_exp_f32_e32 v196, v84
	v_exp_f32_e32 v197, v85
	v_exp_f32_e32 v200, v86
	v_exp_f32_e32 v201, v87
	v_exp_f32_e32 v194, v88
	v_exp_f32_e32 v195, v89
	ds_read_b128 v[82:85], v90 offset:2560
	ds_read_b128 v[86:89], v90 offset:2576
	global_load_dwordx2 v[202:203], v[98:99], off offset:192
	v_add_u32_e32 v98, s6, v215
	s_cmp_lt_u32 s46, 60
	v_ashrrev_i32_e32 v99, 31, v98
	s_cselect_b64 s[54:55], -1, 0
	s_lshl_b32 s6, s56, 6
	v_lshlrev_b64 v[98:99], 8, v[98:99]
	s_add_i32 s56, s6, 0x100
	s_add_i32 s57, s6, 0xfffff100
	v_lshl_add_u64 v[98:99], s[52:53], 0, v[98:99]
	s_and_b64 s[52:53], s[54:55], exec
	s_cselect_b32 s54, s56, s57
	v_lshl_add_u64 v[220:221], v[98:99], 0, v[178:179]
	v_add_u32_e32 v98, s54, v215
	v_ashrrev_i32_e32 v99, 31, v98
	s_cselect_b32 s53, s21, s48
	s_cselect_b32 s52, s20, s47
	v_lshlrev_b64 v[98:99], 8, v[98:99]
	v_lshl_add_u64 v[100:101], v[182:183], 0, s[6:7]
	v_lshl_add_u64 v[98:99], s[52:53], 0, v[98:99]
	global_load_dwordx2 v[204:205], v[100:101], off offset:256
	v_lshl_add_u64 v[222:223], v[98:99], 0, v[178:179]
	s_waitcnt lgkmcnt(0)
; DI f32x16 mfma8(v8i a, v8i b, f32x16 c) { return __builtin_amdgcn_mfma_scale_f32_32x32x64_f8f6f4(a, b, c, 0, 0, 0, 0, 0, 0); }
; DI void attn_unit_d8(unsigned char* lds, const AttnArgs& a) {
;     ...
;     auto tile = [&](const unsigned char* Kb, const unsigned char* Kn, v8i& Pa, v8i& Pb, v8i& v0, v8i& v1, const v8i& Qa, const v8i& Qb, const v8i& w0, const v8i& w1) __attribute__((always_inline)) {
;         qk(Kb, 1, s1a, s1b);
;         v0 = rd32(Kb + voff); v1 = rd32(Kb + voff + 32 * A8_PITCH);
;         o0[0] = mfma8(w0, Qa, o0[0]); o1[0] = mfma8(w0, Qb, o1[0]); o0[1] = mfma8(w1, Qa, o0[1]); o1[1] = mfma8(w1, Qb, o1[1]);
;         expsum(s0a, l0); expsum(s0b, l1); pack4(s0a, Pa, 0); pack4(s0b, Pb, 0);
;         qk(Kn, 0, s0a, s0b);
;         expsum(s1a, l0); expsum(s1b, l1); pack4(s1a, Pa, 4); pack4(s1b, Pb, 4);
; #pragma unroll
;         for (int i = 0; i < 8; ++i) { __builtin_amdgcn_sched_group_barrier(0x008, 1, 0); __builtin_amdgcn_sched_group_barrier(0x402, 22, 0); }
	v_mfma_f32_32x32x64_f8f6f4 v[98:113], v[82:89], v[114:121], 0
	v_exp_f32_e32 v193, v91
	v_exp_f32_e32 v224, v92
	v_exp_f32_e32 v225, v93
	v_exp_f32_e32 v226, v94
	v_exp_f32_e32 v227, v95
	v_exp_f32_e32 v228, v96
	v_exp_f32_e32 v229, v97
	ds_read_b128 v[170:173], v90 offset:5120
	ds_read_b128 v[174:177], v90 offset:5136
	ds_read_b128 v[162:165], v90 offset:7680
	ds_read_b128 v[166:169], v90 offset:7696
	v_pk_add_f32 v[90:91], v[186:187], v[198:199]
	v_pk_add_f32 v[92:93], v[184:185], v[196:197]
	v_pk_add_f32 v[90:91], v[200:201], v[90:91]
	v_pk_add_f32 v[92:93], v[194:195], v[92:93]
	v_pk_add_f32 v[90:91], v[192:193], v[90:91]
	v_pk_add_f32 v[92:93], v[224:225], v[92:93]
	v_exp_f32_e32 v66, v66
	v_exp_f32_e32 v67, v67
	v_exp_f32_e32 v68, v68
	v_exp_f32_e32 v69, v69
	v_exp_f32_e32 v70, v70
	v_exp_f32_e32 v71, v71
	v_exp_f32_e32 v72, v72
	v_pk_add_f32 v[230:231], v[228:229], v[92:93]
	v_pk_add_f32 v[232:233], v[226:227], v[90:91]
	v_mfma_f32_32x32x64_f8f6f4 v[82:97], v[82:89], v[122:129], 0
	v_exp_f32_e32 v73, v73
	v_exp_f32_e32 v74, v74
	v_exp_f32_e32 v75, v75
	v_exp_f32_e32 v76, v76
	v_exp_f32_e32 v77, v77
	v_exp_f32_e32 v78, v78
	v_exp_f32_e32 v79, v79
	v_exp_f32_e32 v80, v80
	v_exp_f32_e32 v81, v81
	v_pk_add_f32 v[186:187], v[190:191], v[66:67]
	v_pk_add_f32 v[188:189], v[188:189], v[68:69]
	s_nop 0
	v_pk_add_f32 v[186:187], v[70:71], v[186:187]
	v_pk_add_f32 v[188:189], v[72:73], v[188:189]
	s_nop 0
	v_cvt_scalef32_pk_fp8_f32 v184, v198, v199, s36
	v_pk_add_f32 v[186:187], v[74:75], v[186:187]
	v_pk_add_f32 v[188:189], v[76:77], v[188:189]
	v_cvt_scalef32_pk_fp8_f32 v185, v200, v201, s36
	v_cvt_scalef32_pk_fp8_f32 v184, v196, v197, s36 op_sel:[0,0,0,1]
	v_pk_add_f32 v[190:191], v[78:79], v[186:187]
	v_pk_add_f32 v[188:189], v[80:81], v[188:189]
	v_mfma_f32_32x32x64_f8f6f4 v[2:17], v[154:161], v[130:137], v[2:17]
	s_nop 0
	s_nop 0
	s_nop 0
	s_nop 0
	s_nop 0
	s_nop 0
	s_mulk_i32 s18, 0x2800
	v_cvt_scalef32_pk_fp8_f32 v186, v192, v193, s36
	v_cvt_scalef32_pk_fp8_f32 v187, v226, v227, s36
	v_cvt_scalef32_pk_fp8_f32 v154, v66, v67, s36
	v_cvt_scalef32_pk_fp8_f32 v155, v70, v71, s36
	v_cvt_scalef32_pk_fp8_f32 v156, v74, v75, s36
	v_cvt_scalef32_pk_fp8_f32 v157, v78, v79, s36
	v_cvt_scalef32_pk_fp8_f32 v185, v194, v195, s36 op_sel:[0,0,0,1]
	v_add_u32_e32 v219, s18, v218
	v_cvt_scalef32_pk_fp8_f32 v186, v224, v225, s36 op_sel:[0,0,0,1]
	v_cvt_scalef32_pk_fp8_f32 v187, v228, v229, s36 op_sel:[0,0,0,1]
	v_cvt_scalef32_pk_fp8_f32 v154, v68, v69, s36 op_sel:[0,0,0,1]
	v_cvt_scalef32_pk_fp8_f32 v155, v72, v73, s36 op_sel:[0,0,0,1]
	v_cvt_scalef32_pk_fp8_f32 v156, v76, v77, s36 op_sel:[0,0,0,1]
	v_cvt_scalef32_pk_fp8_f32 v157, v80, v81, s36 op_sel:[0,0,0,1]
	v_exp_f32_e32 v98, v98
	v_exp_f32_e32 v99, v99
	v_mfma_f32_32x32x64_f8f6f4 v[34:49], v[146:153], v[138:145], v[34:49]
	v_exp_f32_e32 v100, v100
	v_exp_f32_e32 v101, v101
	v_exp_f32_e32 v102, v102
	v_exp_f32_e32 v103, v103
	v_exp_f32_e32 v104, v104
	v_exp_f32_e32 v105, v105
	v_exp_f32_e32 v106, v106
	v_exp_f32_e32 v107, v107
	v_exp_f32_e32 v108, v108
	v_exp_f32_e32 v109, v109
	v_exp_f32_e32 v110, v110
	v_exp_f32_e32 v111, v111
	v_exp_f32_e32 v112, v112
	v_exp_f32_e32 v113, v113
	ds_read_b128 v[192:195], v219
	ds_read_b128 v[196:199], v219 offset:16
	v_pk_add_f32 v[66:67], v[232:233], v[98:99]
	v_pk_add_f32 v[68:69], v[230:231], v[100:101]
	v_pk_add_f32 v[66:67], v[102:103], v[66:67]
	v_pk_add_f32 v[68:69], v[104:105], v[68:69]
	v_pk_add_f32 v[66:67], v[106:107], v[66:67]
	v_pk_add_f32 v[68:69], v[108:109], v[68:69]
	v_pk_add_f32 v[140:141], v[110:111], v[66:67]
	v_pk_add_f32 v[138:139], v[112:113], v[68:69]
	v_mfma_f32_32x32x64_f8f6f4 v[18:33], v[146:153], v[130:137], v[18:33]
	v_exp_f32_e32 v82, v82
	v_exp_f32_e32 v83, v83
	v_exp_f32_e32 v84, v84
	v_exp_f32_e32 v85, v85
	v_exp_f32_e32 v86, v86
	v_exp_f32_e32 v87, v87
	v_exp_f32_e32 v88, v88
	v_exp_f32_e32 v89, v89
	v_exp_f32_e32 v90, v90
	v_exp_f32_e32 v91, v91
	v_exp_f32_e32 v92, v92
	v_exp_f32_e32 v93, v93
	v_exp_f32_e32 v94, v94
	v_exp_f32_e32 v95, v95
	v_exp_f32_e32 v96, v96
	v_exp_f32_e32 v97, v97
	v_pk_add_f32 v[66:67], v[190:191], v[82:83]
	v_pk_add_f32 v[68:69], v[188:189], v[84:85]
	v_pk_add_f32 v[66:67], v[86:87], v[66:67]
	v_pk_add_f32 v[68:69], v[88:89], v[68:69]
	v_pk_add_f32 v[130:131], v[90:91], v[66:67]
	v_pk_add_f32 v[132:133], v[92:93], v[68:69]
	s_waitcnt lgkmcnt(0)
	v_mfma_f32_32x32x64_f8f6f4 v[66:81], v[192:199], v[114:121], 0
	s_nop 0
	s_nop 0
	s_nop 0
	s_nop 0
	s_nop 0
	s_nop 0
	s_nop 0
	v_cvt_scalef32_pk_fp8_f32 v188, v98, v99, s36
	v_cvt_scalef32_pk_fp8_f32 v189, v102, v103, s36
	v_cvt_scalef32_pk_fp8_f32 v190, v106, v107, s36
	v_cvt_scalef32_pk_fp8_f32 v191, v110, v111, s36
	v_cvt_scalef32_pk_fp8_f32 v158, v82, v83, s36
	v_cvt_scalef32_pk_fp8_f32 v159, v86, v87, s36
	v_pk_add_f32 v[142:143], v[96:97], v[132:133]
	v_pk_add_f32 v[144:145], v[94:95], v[130:131]
	v_cvt_scalef32_pk_fp8_f32 v160, v90, v91, s36
	v_cvt_scalef32_pk_fp8_f32 v188, v100, v101, s36 op_sel:[0,0,0,1]
	v_cvt_scalef32_pk_fp8_f32 v189, v104, v105, s36 op_sel:[0,0,0,1]
	v_cvt_scalef32_pk_fp8_f32 v190, v108, v109, s36 op_sel:[0,0,0,1]
	v_cvt_scalef32_pk_fp8_f32 v191, v112, v113, s36 op_sel:[0,0,0,1]
	v_cvt_scalef32_pk_fp8_f32 v158, v84, v85, s36 op_sel:[0,0,0,1]
	v_cvt_scalef32_pk_fp8_f32 v159, v88, v89, s36 op_sel:[0,0,0,1]
	v_mfma_f32_32x32x64_f8f6f4 v[98:113], v[192:199], v[122:129], 0
	global_load_dwordx2 v[192:193], v[220:221], off
	global_load_dwordx2 v[194:195], v[222:223], off
	ds_read_b128 v[130:133], v219 offset:2560
	ds_read_b128 v[134:137], v219 offset:2576
	s_mulk_i32 s19, 0x2800
	s_nop 0
	v_exp_f32_e32 v146, v66
	v_exp_f32_e32 v147, v67
	v_exp_f32_e32 v148, v68
	v_exp_f32_e32 v149, v69
	s_add_i32 s19, s19, 0
	v_cvt_scalef32_pk_fp8_f32 v161, v94, v95, s36
	v_exp_f32_e32 v150, v70
	v_exp_f32_e32 v151, v71
	v_exp_f32_e32 v152, v72
	v_exp_f32_e32 v153, v73
	v_add_u32_e32 v224, s19, v216
	v_add_u32_e32 v225, s19, v217
	v_cvt_scalef32_pk_fp8_f32 v160, v92, v93, s36 op_sel:[0,0,0,1]
	v_cvt_scalef32_pk_fp8_f32 v161, v96, v97, s36 op_sel:[0,0,0,1]
	v_exp_f32_e32 v196, v74
	v_exp_f32_e32 v197, v75
	v_exp_f32_e32 v198, v76
	v_exp_f32_e32 v199, v77
	v_exp_f32_e32 v200, v78
	v_exp_f32_e32 v201, v79
	v_exp_f32_e32 v220, v80
	v_exp_f32_e32 v221, v81
	s_waitcnt lgkmcnt(0)
; DI unsigned pk4_fp8_mul64(float a, float b, float c, float d) { v2s_t r = {0, 0}; r = __builtin_amdgcn_cvt_scalef32_pk_fp8_f32(r, a, b, 0.015625f, false); r = __builtin_amdgcn_cvt_scalef32_pk_fp8_f32(r, c, d, 0.015625f, true); return __builtin_bit_cast(unsigned, r); }
; DI f32x16 mfma8(v8i a, v8i b, f32x16 c) { return __builtin_amdgcn_mfma_scale_f32_32x32x64_f8f6f4(a, b, c, 0, 0, 0, 0, 0, 0); }
; DI void attn_unit_a8(unsigned char* lds, const AttnArgs& a) {
;     ...
;     auto w_cvt = [&]() __attribute__((always_inline)) { unsigned char* t8 = lds + AT_WT + wn4 * WPITCH + 4 * wid;
; #pragma unroll
;         for (int j = 0; j < 4; ++j) *(unsigned*)(t8 + j * WPITCH) = pk4_fp8_mul64(wq[0][j], wq[1][j], wq[2][j], wq[3][j]); };
; DI void attn_unit_d8(unsigned char* lds, const AttnArgs& a) {
;     ...
;     auto tile = [&](const unsigned char* Kb, const unsigned char* Kn, v8i& Pa, v8i& Pb, v8i& v0, v8i& v1, const v8i& Qa, const v8i& Qb, const v8i& w0, const v8i& w1) __attribute__((always_inline)) {
;         qk(Kb, 1, s1a, s1b);
;         v0 = rd32(Kb + voff); v1 = rd32(Kb + voff + 32 * A8_PITCH);
;         o0[0] = mfma8(w0, Qa, o0[0]); o1[0] = mfma8(w0, Qb, o1[0]); o0[1] = mfma8(w1, Qa, o0[1]); o1[1] = mfma8(w1, Qb, o1[1]);
;         expsum(s0a, l0); expsum(s0b, l1); pack4(s0a, Pa, 0); pack4(s0b, Pb, 0);
;         qk(Kn, 0, s0a, s0b);
;         expsum(s1a, l0); expsum(s1b, l1); pack4(s1a, Pa, 4); pack4(s1b, Pb, 4);
; #pragma unroll
;         for (int i = 0; i < 8; ++i) { __builtin_amdgcn_sched_group_barrier(0x008, 1, 0); __builtin_amdgcn_sched_group_barrier(0x402, 22, 0); }
	v_mfma_f32_32x32x64_f8f6f4 v[82:97], v[130:137], v[114:121], 0
	v_add_f32_e64 v66, v140, v146
	v_add_f32_e64 v67, v141, v147
	v_add_f32_e64 v68, v138, v148
	v_add_f32_e64 v69, v139, v149
	v_add_f32_e64 v66, v150, v66
	v_add_f32_e64 v67, v151, v67
	v_add_f32_e64 v68, v152, v68
	v_add_f32_e64 v69, v153, v69
	v_add_f32_e64 v138, v196, v66
	v_add_f32_e64 v139, v197, v67
	v_add_f32_e64 v140, v198, v68
	v_add_f32_e64 v141, v199, v69
	v_exp_f32_e32 v98, v98
	v_exp_f32_e32 v99, v99
	v_exp_f32_e32 v100, v100
	v_exp_f32_e32 v101, v101
	v_exp_f32_e32 v102, v102
	v_exp_f32_e32 v103, v103
	v_exp_f32_e32 v104, v104
	v_exp_f32_e32 v105, v105
	v_exp_f32_e32 v106, v106
	v_exp_f32_e32 v107, v107
	v_exp_f32_e32 v108, v108
	v_exp_f32_e32 v109, v109
	v_exp_f32_e32 v110, v110
	v_exp_f32_e32 v111, v111
	v_exp_f32_e32 v112, v112
	v_exp_f32_e32 v113, v113
	v_mfma_f32_32x32x64_f8f6f4 v[66:81], v[130:137], v[122:129], 0
	v_add_f32_e64 v130, v144, v98
	v_add_f32_e64 v131, v145, v99
	v_add_f32_e64 v132, v142, v100
	v_add_f32_e64 v133, v143, v101
	v_add_f32_e64 v142, v102, v130
	v_add_f32_e64 v143, v103, v131
	v_add_f32_e64 v132, v104, v132
	v_add_f32_e64 v133, v105, v133
	v_add_f32_e64 v134, v220, v140
	v_add_f32_e64 v135, v221, v141
	v_add_f32_e64 v136, v200, v138
	v_add_f32_e64 v137, v201, v139
	s_nop 0
	s_nop 0
	s_nop 0
	s_nop 0
	s_nop 0
	s_nop 0
	v_pk_add_f32 v[142:143], v[106:107], v[142:143]
	v_pk_add_f32 v[132:133], v[108:109], v[132:133]
	v_cvt_scalef32_pk_fp8_f32 v138, v146, v147, s36
	v_cvt_scalef32_pk_fp8_f32 v139, v150, v151, s36
	v_cvt_scalef32_pk_fp8_f32 v140, v196, v197, s36
	v_cvt_scalef32_pk_fp8_f32 v141, v200, v201, s36
	v_cvt_scalef32_pk_fp8_f32 v130, v98, v99, s36
	v_cvt_scalef32_pk_fp8_f32 v131, v102, v103, s36
	v_pk_add_f32 v[146:147], v[112:113], v[132:133]
	v_pk_add_f32 v[150:151], v[110:111], v[142:143]
	v_mfma_f32_32x32x64_f8f6f4 v[50:65], v[170:177], v[184:191], v[50:65]
	v_exp_f32_e32 v82, v82
	v_exp_f32_e32 v83, v83
	v_exp_f32_e32 v84, v84
	v_exp_f32_e32 v85, v85
	v_add_u32_e32 v102, s17, v218
	v_exp_f32_e32 v86, v86
	v_exp_f32_e32 v87, v87
	v_exp_f32_e32 v88, v88
	v_exp_f32_e32 v89, v89
	v_cvt_scalef32_pk_fp8_f32 v130, v100, v101, s36 op_sel:[0,0,0,1]
	v_cvt_scalef32_pk_fp8_f32 v131, v104, v105, s36 op_sel:[0,0,0,1]
	v_exp_f32_e32 v90, v90
	v_exp_f32_e32 v91, v91
	v_exp_f32_e32 v92, v92
	v_exp_f32_e32 v93, v93
	ds_read_b128 v[98:101], v102
	ds_read_b128 v[102:105], v102 offset:16
	s_nop 0
	v_cvt_scalef32_pk_fp8_f32 v138, v148, v149, s36 op_sel:[0,0,0,1]
	v_cvt_scalef32_pk_fp8_f32 v139, v152, v153, s36 op_sel:[0,0,0,1]
	v_cvt_scalef32_pk_fp8_f32 v140, v198, v199, s36 op_sel:[0,0,0,1]
	v_cvt_scalef32_pk_fp8_f32 v141, v220, v221, s36 op_sel:[0,0,0,1]
	s_nop 0
	v_exp_f32_e32 v94, v94
	v_mfma_f32_32x32x64_f8f6f4 v[2:17], v[170:177], v[154:161], v[2:17]
	v_exp_f32_e32 v148, v96
	v_cvt_scalef32_pk_fp8_f32 v132, v106, v107, s36
	v_exp_f32_e32 v149, v97
	v_pk_add_f32 v[96:97], v[136:137], v[82:83]
	v_pk_add_f32 v[106:107], v[134:135], v[84:85]
	v_exp_f32_e32 v66, v66
	v_exp_f32_e32 v67, v67
	v_exp_f32_e32 v68, v68
	v_exp_f32_e32 v69, v69
	v_exp_f32_e32 v95, v95
	v_cvt_scalef32_pk_fp8_f32 v133, v110, v111, s36
	v_pk_add_f32 v[106:107], v[88:89], v[106:107]
	v_pk_add_f32 v[96:97], v[86:87], v[96:97]
	v_exp_f32_e32 v70, v70
	v_exp_f32_e32 v71, v71
	v_exp_f32_e32 v72, v72
	v_exp_f32_e32 v73, v73
	v_cvt_scalef32_pk_fp8_f32 v132, v108, v109, s36 op_sel:[0,0,0,1]
	v_cvt_scalef32_pk_fp8_f32 v133, v112, v113, s36 op_sel:[0,0,0,1]
	v_pk_add_f32 v[96:97], v[90:91], v[96:97]
	v_pk_add_f32 v[106:107], v[92:93], v[106:107]
	v_exp_f32_e32 v74, v74
	v_mfma_f32_32x32x64_f8f6f4 v[34:49], v[162:169], v[184:191], v[34:49]
	v_exp_f32_e32 v75, v75
	v_exp_f32_e32 v76, v76
	v_exp_f32_e32 v77, v77
	v_exp_f32_e32 v78, v78
	v_exp_f32_e32 v79, v79
	s_nop 0
	v_exp_f32_e32 v80, v80
	v_exp_f32_e32 v81, v81
	s_nop 0
	s_nop 0
	v_cvt_scalef32_pk_fp8_f32 v142, v82, v83, s36
	s_nop 0
	v_cvt_scalef32_pk_fp8_f32 v143, v86, v87, s36
	v_cvt_scalef32_pk_fp8_f32 v144, v90, v91, s36
	v_cvt_scalef32_pk_fp8_f32 v142, v84, v85, s36 op_sel:[0,0,0,1]
	v_pk_add_f32 v[82:83], v[150:151], v[66:67]
	v_pk_add_f32 v[84:85], v[146:147], v[68:69]
	s_mulk_i32 s49, 0x2800
	v_pk_add_f32 v[184:185], v[148:149], v[106:107]
	v_pk_add_f32 v[186:187], v[94:95], v[96:97]
	v_cvt_scalef32_pk_fp8_f32 v145, v94, v95, s36
	v_cvt_scalef32_pk_fp8_f32 v143, v88, v89, s36 op_sel:[0,0,0,1]
	v_cvt_scalef32_pk_fp8_f32 v144, v92, v93, s36 op_sel:[0,0,0,1]
	v_mfma_f32_32x32x64_f8f6f4 v[18:33], v[162:169], v[154:161], v[18:33]
	v_add_f32_e64 v84, v72, v84
	v_add_f32_e64 v85, v73, v85
	v_add_f32_e64 v82, v70, v82
	v_add_f32_e64 v83, v71, v83
	s_nop 0
	s_nop 0
	s_nop 0
	s_nop 0
	s_add_i32 s6, s49, 0
	v_add_f32_e64 v82, v74, v82
	v_add_f32_e64 v83, v75, v83
	v_add_f32_e64 v84, v76, v84
	v_add_f32_e64 v85, v77, v85
	v_cvt_scalef32_pk_fp8_f32 v134, v66, v67, s36
	v_cvt_scalef32_pk_fp8_f32 v135, v70, v71, s36
	v_cvt_scalef32_pk_fp8_f32 v136, v74, v75, s36
	v_cvt_scalef32_pk_fp8_f32 v137, v78, v79, s36
	v_pk_add_f32 v[188:189], v[80:81], v[84:85]
	v_pk_add_f32 v[190:191], v[78:79], v[82:83]
	v_add_u32_e32 v106, s6, v216
	v_add_u32_e32 v107, s6, v217
	v_cvt_scalef32_pk_fp8_f32 v145, v148, v149, s36 op_sel:[0,0,0,1]
	v_cvt_scalef32_pk_fp8_f32 v134, v68, v69, s36 op_sel:[0,0,0,1]
	v_cvt_scalef32_pk_fp8_f32 v135, v72, v73, s36 op_sel:[0,0,0,1]
	v_cvt_scalef32_pk_fp8_f32 v136, v76, v77, s36 op_sel:[0,0,0,1]
	v_cvt_scalef32_pk_fp8_f32 v137, v80, v81, s36 op_sel:[0,0,0,1]
	s_waitcnt lgkmcnt(0)
	v_mfma_f32_32x32x64_f8f6f4 v[82:97], v[98:105], v[114:121], 0
	ds_read_b128 v[154:157], v219 offset:5120
	ds_read_b128 v[158:161], v219 offset:5136
	ds_read_b128 v[146:149], v219 offset:7680
	ds_read_b128 v[150:153], v219 offset:7696
	s_cmpk_gt_i32 s42, 0x1ff
	s_cbranch_scc1 .Lmy_rd0_noc
	s_add_i32 s72, s61, -1
	s_cmp_lt_u32 s72, 24
	s_cbranch_scc0 .Lmy_rd0_noc
	s_waitcnt vmcnt(4)
	v_cvt_scalef32_pk_fp8_f32 v236, v236, v240, s62
	v_cvt_scalef32_pk_fp8_f32 v237, v237, v241, s62
	v_cvt_scalef32_pk_fp8_f32 v238, v238, v242, s62
	v_cvt_scalef32_pk_fp8_f32 v239, v239, v243, s62
	v_cvt_scalef32_pk_fp8_f32 v236, v244, v248, s62 op_sel:[0,0,0,1]
	v_cvt_scalef32_pk_fp8_f32 v237, v245, v249, s62 op_sel:[0,0,0,1]
	v_cvt_scalef32_pk_fp8_f32 v238, v246, v250, s62 op_sel:[0,0,0,1]
	v_cvt_scalef32_pk_fp8_f32 v239, v247, v251, s62 op_sel:[0,0,0,1]
	ds_write_b32 v252, v236
	ds_write_b32 v252, v237 offset:36
	ds_write_b32 v252, v238 offset:72
	ds_write_b32 v252, v239 offset:108
; DI void attn_unit_a8(unsigned char* lds, const AttnArgs& a) {
;     ...
;     auto w_decode = [&](int j, const float*& src, unsigned char*& dst, int& ld, int& n0, int& k0, bool& gu) __attribute__((always_inline)) {
;         const int g = (j >> 2) * 512 + a.wl, e = g / 96, rr = g - e * 96; KParamsPtr kp = kparams();
;         if (rr < 64) { src = kp->w_gu + ((size_t)a.wli * NE + e) * (1024 * 2048); dst = kp->ws + WS_WGU + (size_t)a.wli * SZ_WGU + (size_t)e * 2048 * 1024; ld = 2048; n0 = (rr & 7) * 256; k0 = ((rr >> 3) * 4 + (j & 3)) * 32; gu = true; }
;         else { const int q = rr - 64; src = kp->w_dn + ((size_t)a.wli * NE + e) * (1024 * 1024); dst = kp->ws + WS_WDN + (size_t)a.wli * SZ_WDN + (size_t)e * 1024 * 1024; ld = 1024; n0 = (q & 3) * 256; k0 = ((q >> 2) * 4 + (j & 3)) * 32; gu = false; } };
;     auto w_issue = [&](int j) __attribute__((always_inline)) { const float* src; unsigned char* dst; int ld, n0, k0; bool gu; w_decode(j, src, dst, ld, n0, k0, gu);
;         const float* p = src + (size_t)(k0 + 4 * wid) * ld + n0 + wn4;
;         wq[0] = __builtin_nontemporal_load((const f32x4*)p); wq[1] = __builtin_nontemporal_load((const f32x4*)(p + ld));
;         wq[2] = __builtin_nontemporal_load((const f32x4*)(p + (size_t)2 * ld)); wq[3] = __builtin_nontemporal_load((const f32x4*)(p + (size_t)3 * ld)); };
;     auto w_cvt = [&]() __attribute__((always_inline)) { unsigned char* t8 = lds + AT_WT + wn4 * WPITCH + 4 * wid;
; #pragma unroll
;         for (int j = 0; j < 4; ++j) *(unsigned*)(t8 + j * WPITCH) = pk4_fp8_mul64(wq[0][j], wq[1][j], wq[2][j], wq[3][j]); };
;     const int wcol = tid >> 1, whalf = tid & 1;
;     const unsigned wper_gu = (unsigned)((wcol >> 7) * 256 + (wcol & 96) + invperm32(wcol & 31)) * 1024u + 16u * whalf;
;     const unsigned wper_dn = (unsigned)fwd_lane16(wcol) * 1024u + 16u * whalf;
;     auto w_store = [&](int j) __attribute__((always_inline)) { const float* src; unsigned char* dst; int ld, n0, k0; bool gu; w_decode(j, src, dst, ld, n0, k0, gu);
;         const int nb = n0 >> 8; const unsigned uni = (unsigned)(gu ? (nb & 3) * 512 + (nb >> 2) * 128 : nb * 256) * 1024u + (unsigned)k0;
;         const unsigned off = (gu ? wper_gu : wper_dn) + uni;
;         const unsigned* t = (const unsigned*)(lds + AT_WT + wcol * WPITCH + 16 * whalf);
;         *(u32x4*)(dst + off) = (u32x4){t[0], t[1], t[2], t[3]}; };
.Lmy_rd0_noc:
	ds_read2_b32 v[244:245], v253 offset1:1
	ds_read2_b32 v[246:247], v253 offset0:2 offset1:3
	s_cmpk_gt_i32 s42, 0x1ff
	s_cbranch_scc1 .Lmy_rd0_ldummy
	s_cmp_lt_u32 s61, 24
	s_cbranch_scc0 .Lmy_rd0_ldummy
	s_lshr_b32 s73, s61, 2
	s_lshl_b32 s73, s73, 9
	s_add_i32 s73, s73, s42
	s_mul_i32 s75, s73, 0xaaab
	s_lshr_b32 s75, s75, 22
	s_mul_i32 s76, s75, 0x60
	s_sub_i32 s76, s73, s76
	s_and_b32 s77, s61, 3
	s_add_i32 s75, s75, 0
	s_cmp_lt_u32 s76, 64
	s_cbranch_scc0 .Lmy_rd0_ldn
	s_lshr_b32 s78, s76, 3
	s_lshl_b32 s78, s78, 2
	s_add_i32 s78, s78, s77
	s_lshl_b32 s78, s78, 5
	s_lshl_b32 s79, s63, 2
	s_add_i32 s78, s78, s79
	s_lshl_b32 s78, s78, 13
	s_and_b32 s79, s76, 7
	s_lshl_b32 s79, s79, 10
	s_add_i32 s78, s78, s79
	s_lshl_b32 s79, s75, 23
	s_add_u32 s84, s66, s79
	s_addc_u32 s85, s67, 0
	s_add_u32 s84, s84, s78
	s_addc_u32 s85, s85, 0
	s_movk_i32 s80, 0x2000
	s_branch .Lmy_rd0_lgo
.Lmy_rd0_ldn:
	s_sub_i32 s76, s76, 64
	s_lshr_b32 s78, s76, 2
	s_lshl_b32 s78, s78, 2
	s_add_i32 s78, s78, s77
	s_lshl_b32 s78, s78, 5
	s_lshl_b32 s79, s63, 2
	s_add_i32 s78, s78, s79
	s_lshl_b32 s78, s78, 12
	s_and_b32 s79, s76, 3
	s_lshl_b32 s79, s79, 10
	s_add_i32 s78, s78, s79
	s_lshl_b32 s79, s75, 22
	s_add_u32 s84, s68, s79
	s_addc_u32 s85, s69, 0
	s_add_u32 s84, s84, s78
	s_addc_u32 s85, s85, 0
	s_movk_i32 s80, 0x1000
	s_branch .Lmy_rd0_lgo
.Lmy_rd0_ldummy:
	s_mov_b64 s[84:85], s[70:71]
	s_mov_b32 s80, 0
.Lmy_rd0_lgo:
	global_load_dwordx4 v[236:239], v235, s[84:85] nt
	s_add_u32 s84, s84, s80
	s_addc_u32 s85, s85, 0
	global_load_dwordx4 v[240:243], v235, s[84:85] nt
	s_add_u32 s84, s84, s80
	s_addc_u32 s85, s85, 0
	s_cmpk_gt_i32 s42, 0x1ff
	s_cbranch_scc1 .Lmy_rd0_sdummy
	s_add_i32 s72, s61, -2
	s_cmp_lt_u32 s72, 24
	s_cbranch_scc0 .Lmy_rd0_sdummy
	s_lshr_b32 s73, s72, 2
	s_lshl_b32 s73, s73, 9
	s_add_i32 s73, s73, s42
	s_mul_i32 s75, s73, 0xaaab
	s_lshr_b32 s75, s75, 22
	s_mul_i32 s76, s75, 0x60
	s_sub_i32 s76, s73, s76
	s_and_b32 s77, s72, 3
	s_cmp_lt_u32 s76, 64
	s_cbranch_scc0 .Lmy_rd0_sdn
	s_lshr_b32 s78, s76, 3
	s_lshl_b32 s78, s78, 2
	s_add_i32 s78, s78, s77
	s_lshl_b32 s78, s78, 5
	s_and_b32 s79, s76, 7
	s_and_b32 s81, s79, 3
	s_lshl_b32 s81, s81, 9
	s_lshr_b32 s79, s79, 2
	s_lshl_b32 s79, s79, 7
	s_add_i32 s81, s81, s79
	s_lshl_b32 s81, s81, 10
	s_add_i32 s81, s81, s78
	s_lshl_b32 s79, s75, 21
	s_add_i32 s81, s81, s79
	s_add_u32 s82, s70, 0x1094000
	s_addc_u32 s83, s71, 0
	s_add_u32 s82, s82, s81
	s_addc_u32 s83, s83, 0
	s_waitcnt lgkmcnt(0)
	global_store_dwordx4 v254, v[244:247], s[82:83]
	s_branch .Lmy_rd0_sdone
.Lmy_rd0_sdn:
	s_sub_i32 s76, s76, 64
	s_lshr_b32 s78, s76, 2
	s_lshl_b32 s78, s78, 2
	s_add_i32 s78, s78, s77
	s_lshl_b32 s78, s78, 5
	s_and_b32 s79, s76, 3
	s_lshl_b32 s79, s79, 18
	s_add_i32 s81, s79, s78
	s_lshl_b32 s79, s75, 20
	s_add_i32 s81, s81, s79
	s_add_u32 s82, s70, 0x11094000
	s_addc_u32 s83, s71, 0
	s_add_u32 s82, s82, s81
	s_addc_u32 s83, s83, 0
	s_waitcnt lgkmcnt(0)
	global_store_dwordx4 v255, v[244:247], s[82:83]
	s_branch .Lmy_rd0_sdone
.Lmy_rd0_sdummy:
	s_add_u32 s82, s70, 0x1c094000
	s_addc_u32 s83, s71, 0
	s_waitcnt lgkmcnt(0)
	global_store_dwordx4 v254, v[244:247], s[82:83]
.Lmy_rd0_sdone:
	s_nop 0
	global_load_dwordx4 v[244:247], v235, s[84:85] nt
	s_add_u32 s84, s84, s80
	s_addc_u32 s85, s85, 0
	global_load_dwordx4 v[248:251], v235, s[84:85] nt
	v_xor_b32_e32 v252, 0x4000, v252
	v_xor_b32_e32 v253, 0x4000, v253
	s_add_i32 s61, s61, 1
	s_add_i32 s18, s46, 2
	s_cmpk_lt_u32 s46, 0x42
	s_mov_b32 s46, s18
	s_waitcnt vmcnt(6)
	ds_write_b64 v224, v[192:193]
	v_mfma_f32_32x32x64_f8f6f4 v[66:81], v[98:105], v[122:129], 0
	v_add_u32_e32 v98, 0x1400, v225
	v_add_u32_e32 v99, 0x1400, v107
	ds_write2_b32 v98, v202, v203 offset1:8
	s_waitcnt vmcnt(5)
	ds_write_b64 v106, v[194:195]
	ds_write2_b32 v99, v204, v205 offset1:8
	s_waitcnt lgkmcnt(0)
	s_barrier
	s_cbranch_scc1 .LBB0_663
	s_lshl_b64 s[14:15], s[14:15], 10
	s_add_u32 s6, s8, s14
	s_addc_u32 s15, s9, s15
	s_add_u32 s14, s6, s43
	v_mfma_f32_32x32x64_f8f6f4 v[50:65], v[154:161], v[138:145], v[50:65]
	s_addc_u32 s15, s15, 0
	v_mfma_f32_32x32x64_f8f6f4 v[2:17], v[154:161], v[130:137], v[2:17]
	v_mfma_f32_32x32x64_f8f6f4 v[34:49], v[146:153], v[138:145], v[34:49]
	v_mfma_f32_32x32x64_f8f6f4 v[18:33], v[146:153], v[130:137], v[18:33]
	s_setprio 0
	v_add_f32_e32 v66, v186, v187
	v_add_f32_e32 v66, v184, v66
	v_add_f32_e32 v66, v185, v66
	ds_bpermute_b32 v67, v1, v66
	v_add_f32_e32 v68, v190, v191
	v_add_f32_e32 v68, v188, v68
	v_add_f32_e32 v68, v189, v68
	ds_bpermute_b32 v69, v1, v68
	s_waitcnt lgkmcnt(1)
	v_add_f32_e32 v66, v66, v67
	v_div_scale_f32 v67, s[16:17], v66, v66, s36
	v_rcp_f32_e32 v70, v67
	s_waitcnt lgkmcnt(0)
; DI f32x16 mfma8(v8i a, v8i b, f32x16 c) { return __builtin_amdgcn_mfma_scale_f32_32x32x64_f8f6f4(a, b, c, 0, 0, 0, 0, 0, 0); }
; DI void attn_unit_d8(unsigned char* lds, const AttnArgs& a) {
;     ...
;     o0[0] = mfma8(vY0, PaY, o0[0]); o1[0] = mfma8(vY0, PbY, o1[0]); o0[1] = mfma8(vY1, PaY, o0[1]); o1[1] = mfma8(vY1, PbY, o1[1]);
;     __builtin_amdgcn_s_setprio(0);
;     float lt0 = l0[0] + l0[1] + l0[2] + l0[3]; lt0 += __shfl_xor(lt0, 32);
;     float lt1 = l1[0] + l1[1] + l1[2] + l1[3]; lt1 += __shfl_xor(lt1, 32);
;     unsigned char* op = a.out8 + (size_t)(wid * 32 + r) * 1024 + 4 * h;
;     const float r0 = 16.0f / lt0, r1 = 16.0f * a.lam / lt1;
;     float ss = 0.f;
; #pragma unroll
;     for (int d = 0; d < 2; ++d)
; #pragma unroll
;         for (int i = 0; i < 16; ++i) { const float v = o0[d][i] * r0 - o1[d][i] * r1; o0[d][i] = v; ss += v * v; }
;     ss += __shfl_xor(ss, 32);
;     const float rinv = rsqrtf(ss * (1.0f / 64.0f) + EPS) * a.oscale * CAT_SCALE;
;     f32x4 ggv[2][4];
; #pragma unroll
;     for (int d = 0; d < 2; ++d)
; #pragma unroll
;         for (int g = 0; g < 4; ++g) ggv[d][g] = *(const f32x4*)(a.subg + 32 * d + 8 * g + 4 * h);
	v_add_f32_e32 v68, v68, v69
	v_lshlrev_b32_e32 v178, 2, v214
	s_add_i32 s42, s42, s64
	v_fma_f32 v69, -v67, v70, 1.0
	v_fmac_f32_e32 v70, v69, v70
	v_div_scale_f32 v69, vcc, s36, v66, s36
	v_mul_f32_e32 v71, v69, v70
	v_fma_f32 v72, -v67, v71, v69
	v_fmac_f32_e32 v71, v72, v70
	v_fma_f32 v67, -v67, v71, v69
	v_div_scale_f32 v69, s[16:17], v68, v68, v211
	v_rcp_f32_e32 v72, v69
	v_div_fmas_f32 v67, v67, v70, v71
	v_div_fixup_f32 v66, v67, v66, s36
	s_cmpk_gt_i32 s42, 0x21f
	v_fma_f32 v67, -v69, v72, 1.0
	v_fmac_f32_e32 v72, v67, v72
	v_div_scale_f32 v67, vcc, v211, v68, v211
	v_mul_f32_e32 v70, v67, v72
	v_fma_f32 v71, -v69, v70, v67
	v_fmac_f32_e32 v70, v71, v72
	v_fma_f32 v67, -v69, v70, v67
	v_div_fmas_f32 v67, v67, v72, v70
	v_div_fixup_f32 v68, v67, v68, v211
	v_mul_f32_e32 v2, v2, v68
	v_fma_f32 v50, v50, v66, -v2
	v_mul_f32_e32 v2, v3, v68
	v_fma_f32 v51, v51, v66, -v2
	v_mul_f32_e32 v67, v51, v51
	v_mul_f32_e32 v2, v4, v68
	v_fmac_f32_e32 v67, v50, v50
	v_fma_f32 v52, v52, v66, -v2
	v_mul_f32_e32 v2, v5, v68
	v_fmac_f32_e32 v67, v52, v52
	v_fma_f32 v53, v53, v66, -v2
	v_mul_f32_e32 v2, v6, v68
	v_fmac_f32_e32 v67, v53, v53
	v_fma_f32 v54, v54, v66, -v2
	v_mul_f32_e32 v2, v7, v68
	v_fmac_f32_e32 v67, v54, v54
	v_fma_f32 v55, v55, v66, -v2
	v_mul_f32_e32 v2, v8, v68
	v_fmac_f32_e32 v67, v55, v55
	v_fma_f32 v56, v56, v66, -v2
	v_mul_f32_e32 v2, v9, v68
	v_fmac_f32_e32 v67, v56, v56
	v_fma_f32 v57, v57, v66, -v2
	v_mul_f32_e32 v2, v10, v68
	v_fmac_f32_e32 v67, v57, v57
	v_fma_f32 v58, v58, v66, -v2
	v_mul_f32_e32 v2, v11, v68
	v_fmac_f32_e32 v67, v58, v58
	v_fma_f32 v59, v59, v66, -v2
	v_mul_f32_e32 v2, v12, v68
	v_fmac_f32_e32 v67, v59, v59
	v_fma_f32 v60, v60, v66, -v2
	v_mul_f32_e32 v2, v13, v68
	v_fmac_f32_e32 v67, v60, v60
	v_fma_f32 v61, v61, v66, -v2
	v_mul_f32_e32 v14, v14, v68
	v_fmac_f32_e32 v67, v61, v61
	v_fma_f32 v62, v62, v66, -v14
	v_mul_f32_e32 v14, v15, v68
	v_fmac_f32_e32 v67, v62, v62
	v_fma_f32 v63, v63, v66, -v14
	v_mul_f32_e32 v14, v16, v68
	v_lshlrev_b32_e32 v69, 4, v214
	v_fmac_f32_e32 v67, v63, v63
	v_fma_f32 v64, v64, v66, -v14
	v_mul_f32_e32 v14, v17, v68
	global_load_dwordx4 v[2:5], v69, s[10:11] offset:224
	global_load_dwordx4 v[6:9], v69, s[10:11] offset:32
	global_load_dwordx4 v[10:13], v69, s[10:11]
	v_fmac_f32_e32 v67, v64, v64
	v_fma_f32 v65, v65, v66, -v14
	v_mul_f32_e32 v14, v18, v68
	v_fmac_f32_e32 v67, v65, v65
	v_fma_f32 v70, v34, v66, -v14
	v_mul_f32_e32 v14, v19, v68
	v_fmac_f32_e32 v67, v70, v70
	v_fma_f32 v71, v35, v66, -v14
	v_mul_f32_e32 v14, v20, v68
	v_fmac_f32_e32 v67, v71, v71
	v_fma_f32 v72, v36, v66, -v14
	v_mul_f32_e32 v14, v21, v68
	v_fmac_f32_e32 v67, v72, v72
	v_fma_f32 v73, v37, v66, -v14
	v_mul_f32_e32 v14, v22, v68
	v_fmac_f32_e32 v67, v73, v73
	v_fma_f32 v74, v38, v66, -v14
	v_mul_f32_e32 v14, v23, v68
	v_fmac_f32_e32 v67, v74, v74
	v_fma_f32 v75, v39, v66, -v14
	v_fmac_f32_e32 v67, v75, v75
	v_pk_mul_f32 v[14:15], v[24:25], v[68:69] op_sel_hi:[1,0]
	v_pk_mul_f32 v[22:23], v[32:33], v[68:69] op_sel_hi:[1,0]
	v_pk_fma_f32 v[34:35], v[40:41], v[66:67], v[14:15] op_sel_hi:[1,0,1] neg_lo:[0,0,1] neg_hi:[0,0,1]
	s_nop 0
	v_pk_mul_f32 v[14:15], v[34:35], v[34:35]
	s_nop 0
	v_add_f32_e32 v14, v14, v67
	v_add_f32_e32 v20, v15, v14
	v_pk_mul_f32 v[14:15], v[26:27], v[68:69] op_sel_hi:[1,0]
	s_nop 0
	v_pk_fma_f32 v[36:37], v[42:43], v[66:67], v[14:15] op_sel_hi:[1,0,1] neg_lo:[0,0,1] neg_hi:[0,0,1]
	global_load_dwordx4 v[14:17], v69, s[10:11] offset:64
	v_pk_mul_f32 v[18:19], v[36:37], v[36:37]
	v_pk_fma_f32 v[42:43], v[48:49], v[66:67], v[22:23] op_sel_hi:[1,0,1] neg_lo:[0,0,1] neg_hi:[0,0,1]
	v_add_f32_e32 v18, v18, v20
	v_add_f32_e32 v20, v19, v18
	v_pk_mul_f32 v[18:19], v[28:29], v[68:69] op_sel_hi:[1,0]
	v_pk_mul_f32 v[22:23], v[42:43], v[42:43]
	v_pk_fma_f32 v[38:39], v[44:45], v[66:67], v[18:19] op_sel_hi:[1,0,1] neg_lo:[0,0,1] neg_hi:[0,0,1]
	s_nop 0
	v_pk_mul_f32 v[18:19], v[38:39], v[38:39]
	s_nop 0
	v_add_f32_e32 v18, v18, v20
	v_add_f32_e32 v20, v19, v18
	v_pk_mul_f32 v[18:19], v[30:31], v[68:69] op_sel_hi:[1,0]
	s_nop 0
	v_pk_fma_f32 v[40:41], v[46:47], v[66:67], v[18:19] op_sel_hi:[1,0,1] neg_lo:[0,0,1] neg_hi:[0,0,1]
	s_nop 0
	v_pk_mul_f32 v[18:19], v[40:41], v[40:41]
	s_nop 0
	v_add_f32_e32 v18, v18, v20
	v_add_f32_e32 v24, v19, v18
	v_add_f32_e32 v22, v22, v24
	v_add_f32_e32 v26, v23, v22
	ds_bpermute_b32 v27, v1, v26
	global_load_dwordx4 v[18:21], v69, s[10:11] offset:96
	global_load_dwordx4 v[22:25], v69, s[10:11] offset:192
	s_waitcnt lgkmcnt(0)
; DI unsigned pk4_fp8(float a, float b, float c, float d) { int r = 0; r = __builtin_amdgcn_cvt_pk_fp8_f32(a, b, r, false); r = __builtin_amdgcn_cvt_pk_fp8_f32(c, d, r, true); return (unsigned)r; }
; DI float clamp448(float x) { return __builtin_amdgcn_fmed3f(x, -448.0f, 448.0f); }
; DI void attn_unit_d8(unsigned char* lds, const AttnArgs& a) {
;     ...
;     const float rinv = rsqrtf(ss * (1.0f / 64.0f) + EPS) * a.oscale * CAT_SCALE;
;     f32x4 ggv[2][4];
; #pragma unroll
;     for (int d = 0; d < 2; ++d)
; #pragma unroll
;         for (int g = 0; g < 4; ++g) ggv[d][g] = *(const f32x4*)(a.subg + 32 * d + 8 * g + 4 * h);
;     asm volatile("" : "+v"(ggv[0][0]), "+v"(ggv[1][3]));
; #pragma unroll
;     for (int d = 0; d < 2; ++d)
; #pragma unroll
;         for (int g = 0; g < 4; ++g) { const f32x4 gg = ggv[d][g];
;             *(unsigned*)(op + 32 * d + 8 * g) = pk4_fp8(clamp448(o0[d][4 * g] * rinv * gg[0]), clamp448(o0[d][4 * g + 1] * rinv * gg[1]), clamp448(o0[d][4 * g + 2] * rinv * gg[2]), clamp448(o0[d][4 * g + 3] * rinv * gg[3])); }
	v_add_f32_e32 v26, v26, v27
	v_fmamk_f32 v26, v26, 0x3c800000, v212
	v_mul_f32_e32 v27, 0x4b800000, v26
	v_cmp_gt_f32_e32 vcc, s39, v26
	s_nop 1
	v_cndmask_b32_e32 v30, v26, v27, vcc
	global_load_dwordx4 v[26:29], v69, s[10:11] offset:128
	v_rsq_f32_e32 v32, v30
	v_lshlrev_b64 v[30:31], 10, v[180:181]
	v_lshl_add_u64 v[44:45], s[14:15], 0, v[30:31]
	v_lshl_add_u64 v[44:45], v[44:45], 0, v[178:179]
	v_mul_f32_e32 v30, 0x45800000, v32
	v_cndmask_b32_e32 v30, v32, v30, vcc
	v_mul_f32_e32 v48, 0x3f4ccccd, v30
	global_load_dwordx4 v[30:33], v69, s[10:11] offset:160
	v_mul_f32_e32 v48, 0x41800000, v48
	s_waitcnt vmcnt(5)
	v_mul_f32_e32 v49, v50, v48
	v_mul_f32_e32 v10, v10, v49
	v_mul_f32_e32 v49, v51, v48
	v_mul_f32_e32 v11, v11, v49
	v_mul_f32_e32 v49, v52, v48
	v_med3_f32 v10, v10, s40, v213
	v_med3_f32 v11, v11, s40, v213
	v_mul_f32_e32 v12, v12, v49
	s_nop 0
	v_cvt_pk_fp8_f32 v49, v10, v11
	v_mul_f32_e32 v10, v53, v48
	v_mul_f32_e32 v10, v13, v10
	v_med3_f32 v12, v12, s40, v213
	v_med3_f32 v10, v10, s40, v213
	v_cvt_pk_fp8_f32 v49, v12, v10 op_sel:[0,0,1]
	v_mul_f32_e32 v10, v54, v48
	v_mul_f32_e32 v6, v6, v10
	v_mul_f32_e32 v10, v55, v48
	v_mul_f32_e32 v7, v7, v10
	v_mul_f32_e32 v10, v56, v48
	v_med3_f32 v6, v6, s40, v213
	v_med3_f32 v7, v7, s40, v213
	v_mul_f32_e32 v8, v8, v10
	s_nop 0
	v_cvt_pk_fp8_f32 v10, v6, v7
	v_mul_f32_e32 v6, v57, v48
	v_mul_f32_e32 v6, v9, v6
	v_med3_f32 v8, v8, s40, v213
	v_med3_f32 v6, v6, s40, v213
	v_cvt_pk_fp8_f32 v10, v8, v6 op_sel:[0,0,1]
	v_add_co_u32_e32 v6, vcc, s41, v44
	v_lshl_add_u64 v[46:47], v[44:45], 0, s[12:13]
	s_nop 0
	v_addc_co_u32_e32 v7, vcc, 0, v45, vcc
	global_store_dword v[6:7], v49, off offset:768
	global_store_dword v[46:47], v10, off offset:8
	v_mul_f32_e32 v6, v58, v48
	v_mul_f32_e32 v7, v59, v48
	s_waitcnt vmcnt(6)
	v_mul_f32_e32 v6, v14, v6
	v_mul_f32_e32 v7, v15, v7
	v_med3_f32 v6, v6, s40, v213
	v_med3_f32 v7, v7, s40, v213
	s_nop 0
	v_cvt_pk_fp8_f32 v9, v6, v7
	v_mul_f32_e32 v8, v60, v48
	v_mul_f32_e32 v6, v61, v48
	v_mul_f32_e32 v8, v16, v8
	v_mul_f32_e32 v6, v17, v6
	v_med3_f32 v8, v8, s40, v213
	v_med3_f32 v6, v6, s40, v213
	v_cvt_pk_fp8_f32 v9, v8, v6 op_sel:[0,0,1]
	v_mul_f32_e32 v6, v62, v48
	v_mul_f32_e32 v7, v63, v48
	s_nop 0
	v_mul_f32_e32 v8, v64, v48
	s_nop 0
	s_waitcnt vmcnt(5)
	v_mul_f32_e32 v6, v18, v6
	v_mul_f32_e32 v7, v19, v7
	v_med3_f32 v6, v6, s40, v213
	v_med3_f32 v7, v7, s40, v213
	v_cvt_pk_fp8_f32 v10, v6, v7
	v_mul_f32_e32 v6, v65, v48
	v_mul_f32_e32 v8, v20, v8
	v_mul_f32_e32 v6, v21, v6
	v_med3_f32 v8, v8, s40, v213
	v_med3_f32 v6, v6, s40, v213
	v_cvt_pk_fp8_f32 v10, v8, v6 op_sel:[0,0,1]
	v_mul_f32_e32 v6, v70, v48
	v_mul_f32_e32 v7, v71, v48
	s_waitcnt vmcnt(3)
	v_mul_f32_e32 v6, v26, v6
	v_mul_f32_e32 v7, v27, v7
	v_med3_f32 v6, v6, s40, v213
	v_med3_f32 v7, v7, s40, v213
	v_cvt_pk_fp8_f32 v11, v6, v7
	v_mul_f32_e32 v8, v72, v48
	v_mul_f32_e32 v6, v73, v48
	v_mul_f32_e32 v8, v28, v8
	v_mul_f32_e32 v6, v29, v6
	v_med3_f32 v8, v8, s40, v213
	v_med3_f32 v6, v6, s40, v213
	v_cvt_pk_fp8_f32 v11, v8, v6 op_sel:[0,0,1]
	v_mul_f32_e32 v6, v74, v48
	v_mul_f32_e32 v7, v75, v48
	s_waitcnt vmcnt(2)
	v_mul_f32_e32 v6, v30, v6
	v_mul_f32_e32 v7, v31, v7
	v_med3_f32 v6, v6, s40, v213
	v_med3_f32 v7, v7, s40, v213
	s_nop 0
	v_cvt_pk_fp8_f32 v12, v6, v7
	v_mul_f32_e32 v8, v34, v48
	v_mul_f32_e32 v6, v35, v48
	v_mul_f32_e32 v8, v32, v8
	v_mul_f32_e32 v6, v33, v6
	v_med3_f32 v8, v8, s40, v213
	v_med3_f32 v6, v6, s40, v213
	v_cvt_pk_fp8_f32 v12, v8, v6 op_sel:[0,0,1]
	v_mul_f32_e32 v6, v36, v48
	v_mul_f32_e32 v7, v37, v48
	v_mul_f32_e32 v6, v22, v6
	v_mul_f32_e32 v7, v23, v7
	global_store_dword v[46:47], v9, off offset:16
	global_store_dword v[46:47], v10, off offset:24
	global_store_dword v[46:47], v11, off offset:32
	global_store_dword v[46:47], v12, off offset:40
	v_med3_f32 v6, v6, s40, v213
	v_med3_f32 v7, v7, s40, v213
	s_nop 0
	v_cvt_pk_fp8_f32 v9, v6, v7
	v_mul_f32_e32 v8, v38, v48
	v_mul_f32_e32 v6, v39, v48
	v_mul_f32_e32 v8, v24, v8
	v_mul_f32_e32 v6, v25, v6
	v_med3_f32 v8, v8, s40, v213
	v_med3_f32 v6, v6, s40, v213
	v_cvt_pk_fp8_f32 v9, v8, v6 op_sel:[0,0,1]
	v_mul_f32_e32 v6, v40, v48
	v_mul_f32_e32 v2, v2, v6
	v_mul_f32_e32 v6, v41, v48
	v_mul_f32_e32 v3, v3, v6
	v_mul_f32_e32 v6, v42, v48
	v_med3_f32 v2, v2, s40, v213
	v_med3_f32 v3, v3, s40, v213
	v_mul_f32_e32 v4, v4, v6
	s_nop 0
	v_cvt_pk_fp8_f32 v6, v2, v3
	v_mul_f32_e32 v2, v43, v48
	v_mul_f32_e32 v2, v5, v2
	v_med3_f32 v4, v4, s40, v213
	v_med3_f32 v2, v2, s40, v213
	v_cvt_pk_fp8_f32 v6, v4, v2 op_sel:[0,0,1]
	global_store_dword v[46:47], v9, off offset:48
	global_store_dword v[46:47], v6, off offset:56
	s_cbranch_scc0 .LBB0_656

; DI void attn_unit_a8(unsigned char* lds, const AttnArgs& a) {
;     ...
;     { const bf16_t* qp = a.q + (size_t)(wid * 32 + r) * 256 + 32 * h;
;       const u32x4 q0 = *(const u32x4*)qp, q1 = *(const u32x4*)(qp + 8), q2 = *(const u32x4*)(qp + 16), q3 = *(const u32x4*)(qp + 24);
;       const u32x2 c0 = bf8_to_fp8(q0), c1 = bf8_to_fp8(q1), c2 = bf8_to_fp8(q2), c3 = bf8_to_fp8(q3);
;       qf8 = (v8i){(int)c0.x, (int)c0.y, (int)c1.x, (int)c1.y, (int)c2.x, (int)c2.y, (int)c3.x, (int)c3.y}; }
;     ...
;     const bool wrider = a.wl >= 0;
;     if (wrider) w_issue(0);
.LBB0_694:
	s_ashr_i32 s23, s22, 31
	s_and_b32 s9, s4, 3
	s_lshl_b64 s[12:13], s[22:23], 9
	s_add_u32 s4, s36, s12
	s_addc_u32 s11, s37, s13
	s_lshl_b32 s12, s9, 7
	v_mov_b32_e32 v153, v0
	s_add_u32 s12, s4, s12
	s_addc_u32 s13, s11, 0
	v_readfirstlane_b32 s4, v153
	v_and_b32_e32 v18, 31, v153
	s_ashr_i32 s63, s4, 6
	v_lshl_or_b32 v128, s63, 5, v18
	v_ashrrev_i32_e32 v129, 31, v128
	v_lshlrev_b64 v[2:3], 9, v[128:129]
	v_and_b32_e32 v19, 32, v153
	v_lshl_add_u64 v[2:3], s[12:13], 0, v[2:3]
	v_lshlrev_b32_e32 v106, 1, v19
	v_lshl_add_u64 v[14:15], v[2:3], 0, v[106:107]
	global_load_dwordx4 v[2:5], v[14:15], off offset:48
	global_load_dwordx4 v[6:9], v[14:15], off offset:32
	global_load_dwordx4 v[10:13], v[14:15], off offset:16
	s_nop 0
	global_load_dwordx4 v[14:17], v[14:15], off
	v_lshlrev_b32_e32 v20, 2, v153
	s_cmp_gt_i32 s62, 0x10000
	s_cselect_b64 s[24:25], -1, 0
	s_cmp_lt_i32 s62, 0x10000
	v_and_b32_e32 v20, 0xfc, v20
	s_cbranch_scc1 .LBB0_700
	s_mul_i32 s4, s62, 0xaaab
	s_lshr_b32 s4, s4, 22
	s_mul_i32 s11, s4, 0xffffffa0
	s_add_i32 s11, s11, s62
	s_lshl_b32 s15, s62, 8
	s_mov_b64 s[16:17], s[0:1]
	s_cmp_gt_i32 s11, 63
	s_mov_b64 s[18:19], -1
	s_cbranch_scc0 .LBB0_697
	s_load_dwordx2 s[12:13], s[16:17], 0xc0
	s_lshl_b32 s14, s4, 22
	s_waitcnt lgkmcnt(0)
	s_add_u32 s12, s12, s14
	s_addc_u32 s13, s13, 0
	s_and_b32 s18, s11, 0x7ffffffc
	s_and_b32 s14, s15, 0x300
	s_sub_i32 s57, s18, 64
	s_mov_b64 s[18:19], 0

; DI void attn_unit_a8(unsigned char* lds, const AttnArgs& a) {
;     ...
;     const int wn4 = (tid & 63) * 4;
;     constexpr int WPITCH = 36;
;     auto w_decode = [&](int j, const float*& src, unsigned char*& dst, int& ld, int& n0, int& k0, bool& gu) __attribute__((always_inline)) {
;         const int g = (j >> 2) * 512 + a.wl, e = g / 96, rr = g - e * 96; KParamsPtr kp = kparams();
;         if (rr < 64) { src = kp->w_gu + ((size_t)a.wli * NE + e) * (1024 * 2048); dst = kp->ws + WS_WGU + (size_t)a.wli * SZ_WGU + (size_t)e * 2048 * 1024; ld = 2048; n0 = (rr & 7) * 256; k0 = ((rr >> 3) * 4 + (j & 3)) * 32; gu = true; }
;         else { const int q = rr - 64; src = kp->w_dn + ((size_t)a.wli * NE + e) * (1024 * 1024); dst = kp->ws + WS_WDN + (size_t)a.wli * SZ_WDN + (size_t)e * 1024 * 1024; ld = 1024; n0 = (q & 3) * 256; k0 = ((q >> 2) * 4 + (j & 3)) * 32; gu = false; } };
;     auto w_issue = [&](int j) __attribute__((always_inline)) { const float* src; unsigned char* dst; int ld, n0, k0; bool gu; w_decode(j, src, dst, ld, n0, k0, gu);
;         const float* p = src + (size_t)(k0 + 4 * wid) * ld + n0 + wn4;
;         wq[0] = __builtin_nontemporal_load((const f32x4*)p); wq[1] = __builtin_nontemporal_load((const f32x4*)(p + ld));
;         wq[2] = __builtin_nontemporal_load((const f32x4*)(p + (size_t)2 * ld)); wq[3] = __builtin_nontemporal_load((const f32x4*)(p + (size_t)3 * ld)); };
;     auto w_cvt = [&]() __attribute__((always_inline)) { unsigned char* t8 = lds + AT_WT + wn4 * WPITCH + 4 * wid;
; #pragma unroll
;         for (int j = 0; j < 4; ++j) *(unsigned*)(t8 + j * WPITCH) = pk4_fp8_mul64(wq[0][j], wq[1][j], wq[2][j], wq[3][j]); };
;     const int wcol = tid >> 1, whalf = tid & 1;
;     const unsigned wper_gu = (unsigned)((wcol >> 7) * 256 + (wcol & 96) + invperm32(wcol & 31)) * 1024u + 16u * whalf;
;     const unsigned wper_dn = (unsigned)fwd_lane16(wcol) * 1024u + 16u * whalf;
; template <int li>
; DI void layer_phases(unsigned char* smem, LAS unsigned char* ldsL, const int lo, const int hi) {
;     ...
;               const float lam_init = 0.8f - 0.6f * __expf(-0.3f * (float)li);
;               float lam;
;               { const float* dl = kp->d_lambda + li * 128; float a = 0.f, b = 0.f; if (lane < 32) { a = dl[lane] * dl[32 + lane]; b = dl[64 + lane] * dl[96 + lane]; }
;                 lam = __expf(wave_sum(a)) - __expf(wave_sum(b)) + lam_init; }
.LBB0_1883:
	s_or_b64 exec, exec, s[8:9]
	v_mbcnt_lo_u32_b32 v1, -1, 0
	v_mbcnt_hi_u32_b32 v5, -1, v1
	v_and_b32_e32 v1, 64, v5
	v_add_u32_e32 v6, 64, v1
	v_xor_b32_e32 v1, 32, v5
	v_cmp_lt_i32_e32 vcc, v1, v6
	v_xor_b32_e32 v7, 16, v5
	s_and_b32 s5, 0xffff, s5
	v_cndmask_b32_e32 v1, v5, v1, vcc
	v_lshlrev_b32_e32 v1, 2, v1
	ds_bpermute_b32 v4, v1, v3
	v_cmp_lt_i32_e32 vcc, v7, v6
	ds_bpermute_b32 v8, v1, v2
	s_cmp_lg_u32 s5, 0
	s_cselect_b64 s[8:9], -1, 0
	s_waitcnt lgkmcnt(1)
	v_add_f32_e32 v3, v3, v4
	v_cndmask_b32_e32 v4, v5, v7, vcc
	v_lshlrev_b32_e32 v208, 2, v4
	ds_bpermute_b32 v4, v208, v3
	v_xor_b32_e32 v7, 8, v5
	v_cmp_lt_i32_e32 vcc, v7, v6
	s_waitcnt lgkmcnt(1)
	v_add_f32_e32 v2, v2, v8
	s_cmp_lg_u64 s[8:9], 0
	s_waitcnt lgkmcnt(0)
	v_add_f32_e32 v3, v3, v4
	v_cndmask_b32_e32 v4, v5, v7, vcc
	v_lshlrev_b32_e32 v209, 2, v4
	ds_bpermute_b32 v4, v209, v3
	v_xor_b32_e32 v7, 4, v5
	v_cmp_lt_i32_e32 vcc, v7, v6
	s_addc_u32 s60, s4, 0
	s_mov_b32 s9, 0
	s_waitcnt lgkmcnt(0)
	v_add_f32_e32 v3, v3, v4
	v_cndmask_b32_e32 v4, v5, v7, vcc
	ds_bpermute_b32 v7, v208, v2
	v_lshlrev_b32_e32 v210, 2, v4
	ds_bpermute_b32 v4, v210, v3
	s_waitcnt lgkmcnt(1)
	v_add_f32_e32 v2, v2, v7
	ds_bpermute_b32 v7, v209, v2
	s_waitcnt lgkmcnt(1)
	v_add_f32_e32 v3, v3, v4
	v_xor_b32_e32 v4, 2, v5
	v_cmp_lt_i32_e32 vcc, v4, v6
	s_waitcnt lgkmcnt(0)
	v_add_f32_e32 v2, v2, v7
	ds_bpermute_b32 v7, v210, v2
	v_cndmask_b32_e32 v4, v5, v4, vcc
	v_lshlrev_b32_e32 v211, 2, v4
	ds_bpermute_b32 v4, v211, v3
	s_waitcnt lgkmcnt(1)
	v_add_f32_e32 v2, v2, v7
	ds_bpermute_b32 v7, v211, v2
	s_waitcnt lgkmcnt(1)
	v_add_f32_e32 v4, v3, v4
	v_xor_b32_e32 v3, 1, v5
	v_cmp_lt_i32_e32 vcc, v3, v6
	s_waitcnt lgkmcnt(0)
	v_add_f32_e32 v2, v2, v7
	v_cndmask_b32_e32 v3, v5, v3, vcc
	v_lshlrev_b32_e32 v212, 2, v3
	ds_bpermute_b32 v5, v212, v4
	ds_bpermute_b32 v3, v212, v2
	s_and_b64 vcc, exec, s[6:7]
	s_cbranch_vccnz .LBB0_1890
	s_load_dwordx2 s[10:11], s[12:13], 0xd8
	s_waitcnt lgkmcnt(0)
	v_add_f32_e32 v4, v4, v5
	v_add_f32_e32 v2, v2, v3
	v_mul_f32_e32 v4, 0x3fb8aa3b, v4
	v_mul_f32_e32 v2, 0x3fb8aa3b, v2
	v_exp_f32_e32 v6, 0xbedd9914
	v_exp_f32_e32 v4, v4
	v_exp_f32_e32 v2, v2
	s_add_u32 s4, s10, 0x25054000
	s_load_dwordx2 s[12:13], s[12:13], 0x90
	s_addc_u32 s5, s11, 0
	s_add_u32 s24, s10, 0x26154000
	v_mov_b32_e32 v3, 0x3f4ccccd
	s_addc_u32 s25, s11, 0
	v_fmac_f32_e32 v3, 0xbf19999a, v6
	v_sub_f32_e32 v2, v4, v2
	s_add_u32 s28, s10, 0x27ad4000
	v_add_f32_e32 v2, v3, v2
	s_addc_u32 s29, s11, 0
	v_sub_f32_e32 v213, 1.0, v3
	s_mov_b32 s36, 0x41800000
	v_mul_f32_e32 v214, 0x41800000, v2
	s_movk_i32 s37, 0x1100
	v_mov_b32_e32 v179, 0
	s_movk_i32 s38, 0x50
	s_movk_i32 s39, 0x4000
	s_mov_b32 s40, 0x8000
	v_mov_b32_e32 v215, 0x358637bd
	s_mov_b32 s41, 0x800000
	s_mov_b64 s[14:15], 0x2add4300
	s_mov_b32 s42, 0xc3e00000
	s_mov_b32 s43, 0x2add4000
	v_mov_b32_e32 v216, 0x43e00000
	s_mov_b32 s46, s2
	s_load_dwordx2 s[66:67], s[0:1], 0xb0
	s_load_dwordx2 s[68:69], s[0:1], 0xc0
	s_load_dwordx2 s[70:71], s[0:1], 0xd8
	s_mov_b32 s62, 0x3c800000
	v_lshrrev_b32_e32 v236, 6, v0
	v_and_b32_e32 v237, 63, v0
	v_lshlrev_b32_e32 v235, 4, v237
	v_mul_u32_u24_e32 v238, 0x90, v237
	v_lshl_add_u32 v252, v236, 2, v238
	v_add_u32_e32 v252, 0x14000, v252
	v_lshrrev_b32_e32 v239, 1, v0
	v_and_b32_e32 v240, 1, v0
	v_mul_u32_u24_e32 v253, 36, v239
	v_lshl_add_u32 v253, v240, 4, v253
	v_add_u32_e32 v253, 0x10000, v253
	v_and_b32_e32 v241, 0x80, v239
	v_lshlrev_b32_e32 v241, 1, v241
	v_and_b32_e32 v242, 0x60, v239
	v_bfe_u32 v243, v239, 2, 1
	v_bfe_u32 v244, v239, 3, 2
	v_and_b32_e32 v245, 3, v239
	v_lshl_or_b32 v245, v243, 4, v245
	v_lshl_or_b32 v245, v244, 2, v245
	v_add3_u32 v241, v241, v242, v245
	v_lshlrev_b32_e32 v254, 10, v241
	v_lshl_or_b32 v254, v240, 4, v254
	v_bfe_u32 v241, v239, 3, 1
	v_bfe_u32 v242, v239, 6, 2
	v_bfe_u32 v243, v239, 2, 1
	v_bfe_u32 v244, v239, 4, 2
	v_and_b32_e32 v245, 3, v239
	v_lshl_or_b32 v245, v244, 2, v245
	v_lshl_or_b32 v245, v243, 4, v245
	v_lshl_or_b32 v245, v242, 5, v245
	v_lshl_or_b32 v245, v241, 7, v245
	v_lshlrev_b32_e32 v255, 10, v245
	v_lshl_or_b32 v255, v240, 4, v255
	s_nop 0
	v_readfirstlane_b32 s63, v236
	s_waitcnt lgkmcnt(0)

; DI f32x16 mfma8(v8i a, v8i b, f32x16 c) { return __builtin_amdgcn_mfma_scale_f32_32x32x64_f8f6f4(a, b, c, 0, 0, 0, 0, 0, 0); }
; DI void attn_unit_d8(unsigned char* lds, const AttnArgs& a) {
;     ...
;     qk(lds, 0, s0a, s0b);
;     if (wid >= 4) __builtin_amdgcn_s_setprio(1);
;     int sb = 0;
;     const v8i zz8 = (v8i){0, 0, 0, 0, 0, 0, 0, 0};
;     v8i PaX = zz8, PbX = zz8, PaY = zz8, PbY = zz8, vX0 = zz8, vX1 = zz8, vY0 = zz8, vY1 = zz8;
;     auto tile = [&](const unsigned char* Kb, const unsigned char* Kn, v8i& Pa, v8i& Pb, v8i& v0, v8i& v1, const v8i& Qa, const v8i& Qb, const v8i& w0, const v8i& w1) __attribute__((always_inline)) {
;         qk(Kb, 1, s1a, s1b);
;         v0 = rd32(Kb + voff); v1 = rd32(Kb + voff + 32 * A8_PITCH);
;         o0[0] = mfma8(w0, Qa, o0[0]); o1[0] = mfma8(w0, Qb, o1[0]); o0[1] = mfma8(w1, Qa, o0[1]); o1[1] = mfma8(w1, Qb, o1[1]);
;         expsum(s0a, l0); expsum(s0b, l1); pack4(s0a, Pa, 0); pack4(s0b, Pb, 0);
;         qk(Kn, 0, s0a, s0b);
;         expsum(s1a, l0); expsum(s1b, l1); pack4(s1a, Pa, 4); pack4(s1b, Pb, 4);
; #pragma unroll
;         for (int i = 0; i < 8; ++i) { __builtin_amdgcn_sched_group_barrier(0x008, 1, 0); __builtin_amdgcn_sched_group_barrier(0x402, 22, 0); }
;     };
;     for (int t = a.t0; t < a.t1; t += 2) {
;         const int s1 = sb + 1 >= 5 ? sb - 4 : sb + 1, s2 = sb + 2 >= 5 ? sb - 3 : sb + 2, s3 = sb + 3 >= 5 ? sb - 2 : sb + 3, s4 = sb + 4 >= 5 ? sb - 1 : sb + 4;
;         { const int ta = t + 3, tb = t + 4; gload(ta < a.t1 ? ta : a.t1 - 1, kreg0, vreg0); gload(tb < a.t1 ? tb : a.t1 - 1, kreg1, vreg1); }
;         tile(lds + sb * D8_SLOT, lds + s1 * D8_SLOT, PaX, PbX, vX0, vX1, PaY, PbY, vY0, vY1);
;         tile(lds + s1 * D8_SLOT, lds + s2 * D8_SLOT, PaY, PbY, vY0, vY1, PaX, PbX, vX0, vX1);
.LBB0_1887:
	s_mov_b32 s61, 0
	s_ashr_i32 s21, s20, 31
	s_lshl_b64 s[20:21], s[20:21], 8
	s_add_u32 s8, s24, s20
	s_addc_u32 s20, s25, s21
	s_add_u32 s8, s8, s47
	s_addc_u32 s21, s20, 0
	s_add_u32 s20, s8, 0x800000
	v_mov_b32_e32 v2, 0
	s_addc_u32 s21, s21, 0
	s_mov_b32 s23, 0
	s_mov_b32 s22, -2
	v_mov_b32_e32 v138, 0
	v_mov_b32_e32 v139, 0
	v_mov_b32_e32 v140, 0
	v_mov_b32_e32 v141, 0
	v_mov_b32_e32 v142, 0
	v_mov_b32_e32 v143, 0
	v_mov_b32_e32 v144, 0
	v_mov_b32_e32 v145, 0
	v_mov_b32_e32 v130, 0
	v_mov_b32_e32 v131, 0
	v_mov_b32_e32 v132, 0
	v_mov_b32_e32 v133, 0
	v_mov_b32_e32 v134, 0
	v_mov_b32_e32 v135, 0
	v_mov_b32_e32 v136, 0
	v_mov_b32_e32 v137, 0
	v_mov_b32_e32 v154, 0
	v_mov_b32_e32 v155, 0
	v_mov_b32_e32 v156, 0
	v_mov_b32_e32 v157, 0
	v_mov_b32_e32 v158, 0
	v_mov_b32_e32 v159, 0
	v_mov_b32_e32 v160, 0
	v_mov_b32_e32 v161, 0
	v_mov_b32_e32 v146, 0
	v_mov_b32_e32 v147, 0
	v_mov_b32_e32 v148, 0
	v_mov_b32_e32 v149, 0
	v_mov_b32_e32 v150, 0
	v_mov_b32_e32 v151, 0
	v_mov_b32_e32 v152, 0
	v_mov_b32_e32 v153, 0
	v_mov_b32_e32 v3, v2
	v_mov_b32_e32 v4, v2
	v_mov_b32_e32 v5, v2
	v_mov_b32_e32 v6, v2
	v_mov_b32_e32 v7, v2
	v_mov_b32_e32 v8, v2
	v_mov_b32_e32 v9, v2
	v_mov_b32_e32 v10, v2
	v_mov_b32_e32 v11, v2
	v_mov_b32_e32 v12, v2
	v_mov_b32_e32 v13, v2
	v_mov_b32_e32 v14, v2
	v_mov_b32_e32 v15, v2
	v_mov_b32_e32 v16, v2
	v_mov_b32_e32 v17, v2
	v_mov_b32_e32 v18, v2
	v_mov_b32_e32 v19, v2
	v_mov_b32_e32 v20, v2
	v_mov_b32_e32 v21, v2
	v_mov_b32_e32 v22, v2
	v_mov_b32_e32 v23, v2
	v_mov_b32_e32 v24, v2
	v_mov_b32_e32 v25, v2
	v_mov_b32_e32 v26, v2
	v_mov_b32_e32 v27, v2
	v_mov_b32_e32 v28, v2
	v_mov_b32_e32 v29, v2
	v_mov_b32_e32 v30, v2
	v_mov_b32_e32 v31, v2
	v_mov_b32_e32 v32, v2
	v_mov_b32_e32 v33, v2
	v_mov_b32_e32 v50, v2
	v_mov_b32_e32 v51, v2
	v_mov_b32_e32 v52, v2
	v_mov_b32_e32 v53, v2
	v_mov_b32_e32 v54, v2
	v_mov_b32_e32 v55, v2
	v_mov_b32_e32 v56, v2
	v_mov_b32_e32 v57, v2
	v_mov_b32_e32 v58, v2
	v_mov_b32_e32 v59, v2
	v_mov_b32_e32 v60, v2
	v_mov_b32_e32 v61, v2
	v_mov_b32_e32 v62, v2
	v_mov_b32_e32 v63, v2
	v_mov_b32_e32 v64, v2
	v_mov_b32_e32 v65, v2
	v_mov_b32_e32 v34, v2
	v_mov_b32_e32 v35, v2
	v_mov_b32_e32 v36, v2
	v_mov_b32_e32 v37, v2
	v_mov_b32_e32 v38, v2
	v_mov_b32_e32 v39, v2
	v_mov_b32_e32 v40, v2
	v_mov_b32_e32 v41, v2
	v_mov_b32_e32 v42, v2
	v_mov_b32_e32 v43, v2
	v_mov_b32_e32 v44, v2
	v_mov_b32_e32 v45, v2
	v_mov_b32_e32 v46, v2
	v_mov_b32_e32 v47, v2
	v_mov_b32_e32 v48, v2
	v_mov_b32_e32 v49, v2
	v_mov_b32_e32 v188, v2
	v_mov_b32_e32 v189, v2
	v_mov_b32_e32 v186, v2
	v_mov_b32_e32 v187, v2
	v_mov_b32_e32 v192, v2
	v_mov_b32_e32 v193, v2
	v_mov_b32_e32 v190, v2
	v_mov_b32_e32 v191, v2
.LBB0_1888:
	s_add_i32 s22, s22, 2
	s_mul_i32 s8, s23, 0x2800
	s_cmp_gt_i32 s23, 3
	v_mfma_f32_32x32x64_f8f6f4 v[50:65], v[154:161], v[138:145], v[50:65]
	v_exp_f32_e32 v194, v90
	v_add_u32_e32 v90, s8, v219
	s_cselect_b32 s8, -4, 1
	s_add_i32 s51, s8, s23
	s_cmp_gt_i32 s23, 2
	s_cselect_b32 s8, -3, 2
	s_add_i32 s8, s8, s23
	s_cmp_gt_i32 s23, 1
	s_cselect_b32 s52, -2, 3
	s_add_i32 s52, s52, s23
	s_cmp_gt_i32 s23, 0
	s_cselect_b32 s53, -1, 4
	s_min_u32 s56, s22, 64
	s_add_i32 s53, s53, s23
	s_cmp_lt_u32 s22, 61
	s_mul_i32 s50, s8, 0x2800
	s_mov_b32 s23, s8
	s_cselect_b64 s[54:55], -1, 0
	s_lshl_b32 s8, s56, 6
	s_add_i32 s56, s8, 0xc0
	s_add_i32 s57, s8, 0xfffff0c0
	s_and_b64 s[54:55], s[54:55], exec
	v_lshl_add_u64 v[98:99], v[184:185], 0, s[8:9]
	s_cselect_b32 s8, s56, s57
	s_cselect_b32 s55, s19, s21
	s_cselect_b32 s54, s18, s20
	s_min_u32 s58, s22, 63
	v_exp_f32_e32 v200, v82
	v_exp_f32_e32 v201, v83
	v_exp_f32_e32 v198, v84
	v_exp_f32_e32 v199, v85
	v_exp_f32_e32 v202, v86
	v_exp_f32_e32 v203, v87
	v_exp_f32_e32 v196, v88
	v_exp_f32_e32 v197, v89
	ds_read_b128 v[82:85], v90 offset:2560
	ds_read_b128 v[86:89], v90 offset:2576
	global_load_dwordx2 v[204:205], v[98:99], off offset:192
	v_add_u32_e32 v98, s8, v182
	s_cmp_lt_u32 s22, 60
	v_ashrrev_i32_e32 v99, 31, v98
	s_cselect_b64 s[56:57], -1, 0
	s_lshl_b32 s8, s58, 6
	v_lshlrev_b64 v[98:99], 8, v[98:99]
	s_add_i32 s58, s8, 0x100
	s_add_i32 s59, s8, 0xfffff100
	v_lshl_add_u64 v[98:99], s[54:55], 0, v[98:99]
	s_and_b64 s[54:55], s[56:57], exec
	v_lshl_add_u64 v[100:101], v[184:185], 0, s[8:9]
	s_cselect_b32 s8, s58, s59
	v_lshl_add_u64 v[220:221], v[98:99], 0, v[178:179]
	v_add_u32_e32 v98, s8, v182
	v_ashrrev_i32_e32 v99, 31, v98
	s_cselect_b32 s55, s19, s21
	s_cselect_b32 s54, s18, s20
	v_lshlrev_b64 v[98:99], 8, v[98:99]
	v_lshl_add_u64 v[98:99], s[54:55], 0, v[98:99]
	global_load_dwordx2 v[206:207], v[100:101], off offset:256
	v_lshl_add_u64 v[222:223], v[98:99], 0, v[178:179]
	s_waitcnt lgkmcnt(0)
; DI f32x16 mfma8(v8i a, v8i b, f32x16 c) { return __builtin_amdgcn_mfma_scale_f32_32x32x64_f8f6f4(a, b, c, 0, 0, 0, 0, 0, 0); }
; DI void attn_unit_d8(unsigned char* lds, const AttnArgs& a) {
;     ...
;     auto tile = [&](const unsigned char* Kb, const unsigned char* Kn, v8i& Pa, v8i& Pb, v8i& v0, v8i& v1, const v8i& Qa, const v8i& Qb, const v8i& w0, const v8i& w1) __attribute__((always_inline)) {
;         qk(Kb, 1, s1a, s1b);
;         v0 = rd32(Kb + voff); v1 = rd32(Kb + voff + 32 * A8_PITCH);
;         o0[0] = mfma8(w0, Qa, o0[0]); o1[0] = mfma8(w0, Qb, o1[0]); o0[1] = mfma8(w1, Qa, o0[1]); o1[1] = mfma8(w1, Qb, o1[1]);
;         expsum(s0a, l0); expsum(s0b, l1); pack4(s0a, Pa, 0); pack4(s0b, Pb, 0);
;         qk(Kn, 0, s0a, s0b);
;         expsum(s1a, l0); expsum(s1b, l1); pack4(s1a, Pa, 4); pack4(s1b, Pb, 4);
; #pragma unroll
;         for (int i = 0; i < 8; ++i) { __builtin_amdgcn_sched_group_barrier(0x008, 1, 0); __builtin_amdgcn_sched_group_barrier(0x402, 22, 0); }
	v_mfma_f32_32x32x64_f8f6f4 v[98:113], v[82:89], v[114:121], 0
	v_exp_f32_e32 v195, v91
	v_exp_f32_e32 v224, v92
	v_exp_f32_e32 v225, v93
	v_exp_f32_e32 v226, v94
	v_exp_f32_e32 v227, v95
	v_exp_f32_e32 v228, v96
	v_exp_f32_e32 v229, v97
	ds_read_b128 v[170:173], v90 offset:5120
	ds_read_b128 v[174:177], v90 offset:5136
	ds_read_b128 v[162:165], v90 offset:7680
	ds_read_b128 v[166:169], v90 offset:7696
	v_pk_add_f32 v[90:91], v[188:189], v[200:201]
	v_pk_add_f32 v[92:93], v[186:187], v[198:199]
	v_pk_add_f32 v[90:91], v[202:203], v[90:91]
	v_pk_add_f32 v[92:93], v[196:197], v[92:93]
	v_pk_add_f32 v[90:91], v[194:195], v[90:91]
	v_pk_add_f32 v[92:93], v[224:225], v[92:93]
	v_exp_f32_e32 v66, v66
	v_exp_f32_e32 v67, v67
	v_exp_f32_e32 v68, v68
	v_exp_f32_e32 v69, v69
	v_exp_f32_e32 v70, v70
	v_exp_f32_e32 v71, v71
	v_exp_f32_e32 v72, v72
	v_pk_add_f32 v[230:231], v[228:229], v[92:93]
	v_pk_add_f32 v[232:233], v[226:227], v[90:91]
	v_mfma_f32_32x32x64_f8f6f4 v[82:97], v[82:89], v[122:129], 0
	v_exp_f32_e32 v73, v73
	v_exp_f32_e32 v74, v74
	v_exp_f32_e32 v75, v75
	v_exp_f32_e32 v76, v76
	v_exp_f32_e32 v77, v77
	v_exp_f32_e32 v78, v78
	v_exp_f32_e32 v79, v79
	v_exp_f32_e32 v80, v80
	v_exp_f32_e32 v81, v81
	v_pk_add_f32 v[188:189], v[192:193], v[66:67]
	v_pk_add_f32 v[190:191], v[190:191], v[68:69]
	s_nop 0
	v_pk_add_f32 v[188:189], v[70:71], v[188:189]
	v_pk_add_f32 v[190:191], v[72:73], v[190:191]
	s_nop 0
	v_cvt_scalef32_pk_fp8_f32 v186, v200, v201, s36
	v_pk_add_f32 v[188:189], v[74:75], v[188:189]
	v_pk_add_f32 v[190:191], v[76:77], v[190:191]
	v_cvt_scalef32_pk_fp8_f32 v187, v202, v203, s36
	v_cvt_scalef32_pk_fp8_f32 v186, v198, v199, s36 op_sel:[0,0,0,1]
	v_pk_add_f32 v[192:193], v[78:79], v[188:189]
	v_pk_add_f32 v[190:191], v[80:81], v[190:191]
	v_mfma_f32_32x32x64_f8f6f4 v[2:17], v[154:161], v[130:137], v[2:17]
	s_nop 0
	s_nop 0
	s_nop 0
	s_nop 0
	s_nop 0
	s_nop 0
	s_mulk_i32 s51, 0x2800
	v_cvt_scalef32_pk_fp8_f32 v188, v194, v195, s36
	v_cvt_scalef32_pk_fp8_f32 v189, v226, v227, s36
	v_cvt_scalef32_pk_fp8_f32 v154, v66, v67, s36
	v_cvt_scalef32_pk_fp8_f32 v155, v70, v71, s36
	v_cvt_scalef32_pk_fp8_f32 v156, v74, v75, s36
	v_cvt_scalef32_pk_fp8_f32 v157, v78, v79, s36
	v_cvt_scalef32_pk_fp8_f32 v187, v196, v197, s36 op_sel:[0,0,0,1]
	v_add_u32_e32 v234, s51, v219
	v_cvt_scalef32_pk_fp8_f32 v188, v224, v225, s36 op_sel:[0,0,0,1]
	v_cvt_scalef32_pk_fp8_f32 v189, v228, v229, s36 op_sel:[0,0,0,1]
	v_cvt_scalef32_pk_fp8_f32 v154, v68, v69, s36 op_sel:[0,0,0,1]
	v_cvt_scalef32_pk_fp8_f32 v155, v72, v73, s36 op_sel:[0,0,0,1]
	v_cvt_scalef32_pk_fp8_f32 v156, v76, v77, s36 op_sel:[0,0,0,1]
	v_cvt_scalef32_pk_fp8_f32 v157, v80, v81, s36 op_sel:[0,0,0,1]
	v_exp_f32_e32 v98, v98
	v_exp_f32_e32 v99, v99
	v_mfma_f32_32x32x64_f8f6f4 v[34:49], v[146:153], v[138:145], v[34:49]
	v_exp_f32_e32 v100, v100
	v_exp_f32_e32 v101, v101
	v_exp_f32_e32 v102, v102
	v_exp_f32_e32 v103, v103
	v_exp_f32_e32 v104, v104
	v_exp_f32_e32 v105, v105
	v_exp_f32_e32 v106, v106
	v_exp_f32_e32 v107, v107
	v_exp_f32_e32 v108, v108
	v_exp_f32_e32 v109, v109
	v_exp_f32_e32 v110, v110
	v_exp_f32_e32 v111, v111
	v_exp_f32_e32 v112, v112
	v_exp_f32_e32 v113, v113
	ds_read_b128 v[194:197], v234
	ds_read_b128 v[198:201], v234 offset:16
	v_pk_add_f32 v[66:67], v[232:233], v[98:99]
	v_pk_add_f32 v[68:69], v[230:231], v[100:101]
	v_pk_add_f32 v[66:67], v[102:103], v[66:67]
	v_pk_add_f32 v[68:69], v[104:105], v[68:69]
	v_pk_add_f32 v[66:67], v[106:107], v[66:67]
	v_pk_add_f32 v[68:69], v[108:109], v[68:69]
	v_pk_add_f32 v[140:141], v[110:111], v[66:67]
	v_pk_add_f32 v[138:139], v[112:113], v[68:69]
	v_mfma_f32_32x32x64_f8f6f4 v[18:33], v[146:153], v[130:137], v[18:33]
	v_exp_f32_e32 v82, v82
	v_exp_f32_e32 v83, v83
	v_exp_f32_e32 v84, v84
	v_exp_f32_e32 v85, v85
	v_exp_f32_e32 v86, v86
	v_exp_f32_e32 v87, v87
	v_exp_f32_e32 v88, v88
	v_exp_f32_e32 v89, v89
	v_exp_f32_e32 v90, v90
	v_exp_f32_e32 v91, v91
	v_exp_f32_e32 v92, v92
	v_exp_f32_e32 v93, v93
	v_exp_f32_e32 v94, v94
	v_exp_f32_e32 v95, v95
	v_exp_f32_e32 v96, v96
	v_exp_f32_e32 v97, v97
	v_pk_add_f32 v[66:67], v[192:193], v[82:83]
	v_pk_add_f32 v[68:69], v[190:191], v[84:85]
	v_pk_add_f32 v[66:67], v[86:87], v[66:67]
	v_pk_add_f32 v[68:69], v[88:89], v[68:69]
	v_pk_add_f32 v[130:131], v[90:91], v[66:67]
	v_pk_add_f32 v[132:133], v[92:93], v[68:69]
	s_waitcnt lgkmcnt(0)
	v_mfma_f32_32x32x64_f8f6f4 v[66:81], v[194:201], v[114:121], 0
	s_nop 0
	s_nop 0
	s_nop 0
	s_nop 0
	s_nop 0
	s_nop 0
	s_nop 0
	v_cvt_scalef32_pk_fp8_f32 v190, v98, v99, s36
	v_cvt_scalef32_pk_fp8_f32 v191, v102, v103, s36
	v_cvt_scalef32_pk_fp8_f32 v192, v106, v107, s36
	v_cvt_scalef32_pk_fp8_f32 v193, v110, v111, s36
	v_cvt_scalef32_pk_fp8_f32 v158, v82, v83, s36
	v_cvt_scalef32_pk_fp8_f32 v159, v86, v87, s36
	v_pk_add_f32 v[142:143], v[96:97], v[132:133]
	v_pk_add_f32 v[144:145], v[94:95], v[130:131]
	v_cvt_scalef32_pk_fp8_f32 v160, v90, v91, s36
	v_cvt_scalef32_pk_fp8_f32 v190, v100, v101, s36 op_sel:[0,0,0,1]
	v_cvt_scalef32_pk_fp8_f32 v191, v104, v105, s36 op_sel:[0,0,0,1]
	v_cvt_scalef32_pk_fp8_f32 v192, v108, v109, s36 op_sel:[0,0,0,1]
	v_cvt_scalef32_pk_fp8_f32 v193, v112, v113, s36 op_sel:[0,0,0,1]
	v_cvt_scalef32_pk_fp8_f32 v158, v84, v85, s36 op_sel:[0,0,0,1]
	v_cvt_scalef32_pk_fp8_f32 v159, v88, v89, s36 op_sel:[0,0,0,1]
	v_mfma_f32_32x32x64_f8f6f4 v[98:113], v[194:201], v[122:129], 0
	global_load_dwordx2 v[194:195], v[220:221], off
	global_load_dwordx2 v[196:197], v[222:223], off
	ds_read_b128 v[130:133], v234 offset:2560
	ds_read_b128 v[134:137], v234 offset:2576
	v_exp_f32_e32 v146, v66
	v_exp_f32_e32 v147, v67
	s_mulk_i32 s52, 0x2800
	s_nop 0
	s_add_i32 s8, s52, 0
	v_cvt_scalef32_pk_fp8_f32 v161, v94, v95, s36
	v_add_u32_e32 v224, s8, v183
	v_cvt_scalef32_pk_fp8_f32 v160, v92, v93, s36 op_sel:[0,0,0,1]
	v_cvt_scalef32_pk_fp8_f32 v161, v96, v97, s36 op_sel:[0,0,0,1]
	v_exp_f32_e32 v148, v68
	v_exp_f32_e32 v149, v69
	v_exp_f32_e32 v150, v70
	v_exp_f32_e32 v151, v71
	v_exp_f32_e32 v152, v72
	v_exp_f32_e32 v153, v73
	v_exp_f32_e32 v198, v74
	v_exp_f32_e32 v199, v75
	v_exp_f32_e32 v200, v76
	v_exp_f32_e32 v201, v77
	v_exp_f32_e32 v202, v78
	v_exp_f32_e32 v203, v79
	v_exp_f32_e32 v220, v80
	v_exp_f32_e32 v221, v81
	v_pk_add_f32 v[66:67], v[140:141], v[146:147]
	s_waitcnt lgkmcnt(0)
; DI unsigned pk4_fp8_mul64(float a, float b, float c, float d) { v2s_t r = {0, 0}; r = __builtin_amdgcn_cvt_scalef32_pk_fp8_f32(r, a, b, 0.015625f, false); r = __builtin_amdgcn_cvt_scalef32_pk_fp8_f32(r, c, d, 0.015625f, true); return __builtin_bit_cast(unsigned, r); }
; DI f32x16 mfma8(v8i a, v8i b, f32x16 c) { return __builtin_amdgcn_mfma_scale_f32_32x32x64_f8f6f4(a, b, c, 0, 0, 0, 0, 0, 0); }
; DI void attn_unit_a8(unsigned char* lds, const AttnArgs& a) {
;     ...
;     auto w_cvt = [&]() __attribute__((always_inline)) { unsigned char* t8 = lds + AT_WT + wn4 * WPITCH + 4 * wid;
; #pragma unroll
;         for (int j = 0; j < 4; ++j) *(unsigned*)(t8 + j * WPITCH) = pk4_fp8_mul64(wq[0][j], wq[1][j], wq[2][j], wq[3][j]); };
; DI void attn_unit_d8(unsigned char* lds, const AttnArgs& a) {
;     ...
;     auto tile = [&](const unsigned char* Kb, const unsigned char* Kn, v8i& Pa, v8i& Pb, v8i& v0, v8i& v1, const v8i& Qa, const v8i& Qb, const v8i& w0, const v8i& w1) __attribute__((always_inline)) {
;         qk(Kb, 1, s1a, s1b);
;         v0 = rd32(Kb + voff); v1 = rd32(Kb + voff + 32 * A8_PITCH);
;         o0[0] = mfma8(w0, Qa, o0[0]); o1[0] = mfma8(w0, Qb, o1[0]); o0[1] = mfma8(w1, Qa, o0[1]); o1[1] = mfma8(w1, Qb, o1[1]);
;         expsum(s0a, l0); expsum(s0b, l1); pack4(s0a, Pa, 0); pack4(s0b, Pb, 0);
;         qk(Kn, 0, s0a, s0b);
;         expsum(s1a, l0); expsum(s1b, l1); pack4(s1a, Pa, 4); pack4(s1b, Pb, 4);
; #pragma unroll
;         for (int i = 0; i < 8; ++i) { __builtin_amdgcn_sched_group_barrier(0x008, 1, 0); __builtin_amdgcn_sched_group_barrier(0x402, 22, 0); }
	v_mfma_f32_32x32x64_f8f6f4 v[82:97], v[130:137], v[114:121], 0
	v_add_f32_e64 v68, v138, v148
	v_add_f32_e64 v69, v139, v149
	v_add_f32_e64 v66, v150, v66
	v_add_f32_e64 v67, v151, v67
	v_add_f32_e64 v68, v152, v68
	v_add_f32_e64 v69, v153, v69
	v_add_f32_e64 v138, v198, v66
	v_add_f32_e64 v139, v199, v67
	v_add_f32_e64 v140, v200, v68
	v_add_f32_e64 v141, v201, v69
	v_exp_f32_e32 v98, v98
	v_exp_f32_e32 v99, v99
	v_exp_f32_e32 v100, v100
	v_exp_f32_e32 v101, v101
	v_exp_f32_e32 v102, v102
	v_exp_f32_e32 v103, v103
	v_exp_f32_e32 v104, v104
	v_exp_f32_e32 v105, v105
	v_exp_f32_e32 v106, v106
	v_exp_f32_e32 v107, v107
	v_exp_f32_e32 v108, v108
	v_exp_f32_e32 v109, v109
	v_exp_f32_e32 v110, v110
	v_exp_f32_e32 v111, v111
	v_exp_f32_e32 v112, v112
	v_exp_f32_e32 v113, v113
	v_exp_f32_e32 v82, v82
	v_mfma_f32_32x32x64_f8f6f4 v[66:81], v[130:137], v[122:129], 0
	v_add_f32_e64 v130, v144, v98
	v_add_f32_e64 v131, v145, v99
	v_add_f32_e64 v132, v142, v100
	v_add_f32_e64 v133, v143, v101
	v_add_f32_e64 v142, v102, v130
	v_add_f32_e64 v143, v103, v131
	v_add_f32_e64 v132, v104, v132
	v_add_f32_e64 v133, v105, v133
	v_add_f32_e64 v134, v220, v140
	v_add_f32_e64 v135, v221, v141
	v_add_f32_e64 v136, v202, v138
	v_add_f32_e64 v137, v203, v139
	s_nop 0
	s_nop 0
	s_nop 0
	s_nop 0
	s_nop 0
	s_nop 0
	v_pk_add_f32 v[142:143], v[106:107], v[142:143]
	v_pk_add_f32 v[132:133], v[108:109], v[132:133]
	v_cvt_scalef32_pk_fp8_f32 v138, v146, v147, s36
	v_cvt_scalef32_pk_fp8_f32 v139, v150, v151, s36
	v_cvt_scalef32_pk_fp8_f32 v140, v198, v199, s36
	v_cvt_scalef32_pk_fp8_f32 v141, v202, v203, s36
	v_cvt_scalef32_pk_fp8_f32 v130, v98, v99, s36
	v_cvt_scalef32_pk_fp8_f32 v131, v102, v103, s36
	v_pk_add_f32 v[146:147], v[112:113], v[132:133]
	v_pk_add_f32 v[150:151], v[110:111], v[142:143]
	v_mfma_f32_32x32x64_f8f6f4 v[50:65], v[170:177], v[186:193], v[50:65]
	v_exp_f32_e32 v83, v83
	v_exp_f32_e32 v84, v84
	v_exp_f32_e32 v85, v85
	v_add_u32_e32 v102, s50, v219
	v_exp_f32_e32 v86, v86
	v_exp_f32_e32 v87, v87
	v_exp_f32_e32 v88, v88
	v_exp_f32_e32 v89, v89
	v_cvt_scalef32_pk_fp8_f32 v130, v100, v101, s36 op_sel:[0,0,0,1]
	v_cvt_scalef32_pk_fp8_f32 v131, v104, v105, s36 op_sel:[0,0,0,1]
	v_exp_f32_e32 v90, v90
	v_exp_f32_e32 v91, v91
	v_exp_f32_e32 v92, v92
	v_exp_f32_e32 v93, v93
	ds_read_b128 v[98:101], v102
	ds_read_b128 v[102:105], v102 offset:16
	s_nop 0
	v_cvt_scalef32_pk_fp8_f32 v138, v148, v149, s36 op_sel:[0,0,0,1]
	v_cvt_scalef32_pk_fp8_f32 v139, v152, v153, s36 op_sel:[0,0,0,1]
	v_cvt_scalef32_pk_fp8_f32 v140, v200, v201, s36 op_sel:[0,0,0,1]
	v_cvt_scalef32_pk_fp8_f32 v141, v220, v221, s36 op_sel:[0,0,0,1]
	s_nop 0
	v_exp_f32_e32 v94, v94
	v_exp_f32_e32 v95, v95
	v_mfma_f32_32x32x64_f8f6f4 v[2:17], v[170:177], v[154:161], v[2:17]
	v_exp_f32_e32 v148, v96
	v_cvt_scalef32_pk_fp8_f32 v132, v106, v107, s36
	v_exp_f32_e32 v149, v97
	v_pk_add_f32 v[96:97], v[136:137], v[82:83]
	v_pk_add_f32 v[106:107], v[134:135], v[84:85]
	v_exp_f32_e32 v66, v66
	v_exp_f32_e32 v67, v67
	v_exp_f32_e32 v68, v68
	v_exp_f32_e32 v69, v69
	v_cvt_scalef32_pk_fp8_f32 v133, v110, v111, s36
	v_pk_add_f32 v[106:107], v[88:89], v[106:107]
	v_pk_add_f32 v[96:97], v[86:87], v[96:97]
	v_exp_f32_e32 v70, v70
	v_exp_f32_e32 v71, v71
	v_exp_f32_e32 v72, v72
	v_exp_f32_e32 v73, v73
	v_cvt_scalef32_pk_fp8_f32 v132, v108, v109, s36 op_sel:[0,0,0,1]
	v_cvt_scalef32_pk_fp8_f32 v133, v112, v113, s36 op_sel:[0,0,0,1]
	v_pk_add_f32 v[96:97], v[90:91], v[96:97]
	v_pk_add_f32 v[106:107], v[92:93], v[106:107]
	v_exp_f32_e32 v74, v74
	v_exp_f32_e32 v75, v75
	v_mfma_f32_32x32x64_f8f6f4 v[34:49], v[162:169], v[186:193], v[34:49]
	v_exp_f32_e32 v76, v76
	v_exp_f32_e32 v77, v77
	v_exp_f32_e32 v78, v78
	v_exp_f32_e32 v79, v79
	s_nop 0
	v_exp_f32_e32 v80, v80
	v_exp_f32_e32 v81, v81
	s_nop 0
	s_nop 0
	v_cvt_scalef32_pk_fp8_f32 v142, v82, v83, s36
	s_nop 0
	v_cvt_scalef32_pk_fp8_f32 v143, v86, v87, s36
	v_cvt_scalef32_pk_fp8_f32 v144, v90, v91, s36
	v_cvt_scalef32_pk_fp8_f32 v142, v84, v85, s36 op_sel:[0,0,0,1]
	v_pk_add_f32 v[82:83], v[150:151], v[66:67]
	v_pk_add_f32 v[84:85], v[146:147], v[68:69]
	s_mulk_i32 s53, 0x2800
	v_pk_add_f32 v[186:187], v[148:149], v[106:107]
	v_pk_add_f32 v[188:189], v[94:95], v[96:97]
	v_cvt_scalef32_pk_fp8_f32 v145, v94, v95, s36
	v_cvt_scalef32_pk_fp8_f32 v143, v88, v89, s36 op_sel:[0,0,0,1]
	v_cvt_scalef32_pk_fp8_f32 v144, v92, v93, s36 op_sel:[0,0,0,1]
	v_pk_add_f32 v[84:85], v[72:73], v[84:85]
	v_mfma_f32_32x32x64_f8f6f4 v[18:33], v[162:169], v[154:161], v[18:33]
	v_add_f32_e64 v82, v70, v82
	v_add_f32_e64 v83, v71, v83
	s_nop 0
	s_nop 0
	s_nop 0
	s_nop 0
	s_add_i32 s51, s53, 0
	v_add_f32_e64 v82, v74, v82
	v_add_f32_e64 v83, v75, v83
	v_add_f32_e64 v84, v76, v84
	v_add_f32_e64 v85, v77, v85
	v_cvt_scalef32_pk_fp8_f32 v134, v66, v67, s36
	v_cvt_scalef32_pk_fp8_f32 v135, v70, v71, s36
	v_cvt_scalef32_pk_fp8_f32 v136, v74, v75, s36
	v_cvt_scalef32_pk_fp8_f32 v137, v78, v79, s36
	v_pk_add_f32 v[190:191], v[80:81], v[84:85]
	v_pk_add_f32 v[192:193], v[78:79], v[82:83]
	v_add_u32_e32 v106, s8, v218
	v_add_u32_e32 v107, s51, v183
	v_cvt_scalef32_pk_fp8_f32 v145, v148, v149, s36 op_sel:[0,0,0,1]
	v_cvt_scalef32_pk_fp8_f32 v134, v68, v69, s36 op_sel:[0,0,0,1]
	v_cvt_scalef32_pk_fp8_f32 v135, v72, v73, s36 op_sel:[0,0,0,1]
	v_cvt_scalef32_pk_fp8_f32 v136, v76, v77, s36 op_sel:[0,0,0,1]
	v_cvt_scalef32_pk_fp8_f32 v137, v80, v81, s36 op_sel:[0,0,0,1]
	s_waitcnt lgkmcnt(0)
	v_mfma_f32_32x32x64_f8f6f4 v[82:97], v[98:105], v[114:121], 0
	ds_read_b128 v[154:157], v234 offset:5120
	ds_read_b128 v[158:161], v234 offset:5136
	ds_read_b128 v[146:149], v234 offset:7680
	ds_read_b128 v[150:153], v234 offset:7696
	s_cmpk_gt_i32 s46, 0x1ff
	s_cbranch_scc1 .Lmy_rd1_noc
	s_add_i32 s72, s61, -1
	s_cmp_lt_u32 s72, 24
	s_cbranch_scc0 .Lmy_rd1_noc
	s_waitcnt vmcnt(4)
	v_cvt_scalef32_pk_fp8_f32 v236, v236, v240, s62
	v_cvt_scalef32_pk_fp8_f32 v237, v237, v241, s62
	v_cvt_scalef32_pk_fp8_f32 v238, v238, v242, s62
	v_cvt_scalef32_pk_fp8_f32 v239, v239, v243, s62
	v_cvt_scalef32_pk_fp8_f32 v236, v244, v248, s62 op_sel:[0,0,0,1]
	v_cvt_scalef32_pk_fp8_f32 v237, v245, v249, s62 op_sel:[0,0,0,1]
	v_cvt_scalef32_pk_fp8_f32 v238, v246, v250, s62 op_sel:[0,0,0,1]
	v_cvt_scalef32_pk_fp8_f32 v239, v247, v251, s62 op_sel:[0,0,0,1]
	ds_write_b32 v252, v236
	ds_write_b32 v252, v237 offset:36
	ds_write_b32 v252, v238 offset:72
	ds_write_b32 v252, v239 offset:108
; DI KParamsPtr kparams() { KParamsPtr p = (KParamsPtr)__builtin_amdgcn_kernarg_segment_ptr(); asm volatile("" : "+s"(p)); return p; }
; DI void attn_unit_a8(unsigned char* lds, const AttnArgs& a) {
;     ...
;     auto w_decode = [&](int j, const float*& src, unsigned char*& dst, int& ld, int& n0, int& k0, bool& gu) __attribute__((always_inline)) {
;         const int g = (j >> 2) * 512 + a.wl, e = g / 96, rr = g - e * 96; KParamsPtr kp = kparams();
;         if (rr < 64) { src = kp->w_gu + ((size_t)a.wli * NE + e) * (1024 * 2048); dst = kp->ws + WS_WGU + (size_t)a.wli * SZ_WGU + (size_t)e * 2048 * 1024; ld = 2048; n0 = (rr & 7) * 256; k0 = ((rr >> 3) * 4 + (j & 3)) * 32; gu = true; }
;         else { const int q = rr - 64; src = kp->w_dn + ((size_t)a.wli * NE + e) * (1024 * 1024); dst = kp->ws + WS_WDN + (size_t)a.wli * SZ_WDN + (size_t)e * 1024 * 1024; ld = 1024; n0 = (q & 3) * 256; k0 = ((q >> 2) * 4 + (j & 3)) * 32; gu = false; } };
;     auto w_issue = [&](int j) __attribute__((always_inline)) { const float* src; unsigned char* dst; int ld, n0, k0; bool gu; w_decode(j, src, dst, ld, n0, k0, gu);
;         const float* p = src + (size_t)(k0 + 4 * wid) * ld + n0 + wn4;
;         wq[0] = __builtin_nontemporal_load((const f32x4*)p); wq[1] = __builtin_nontemporal_load((const f32x4*)(p + ld));
;         wq[2] = __builtin_nontemporal_load((const f32x4*)(p + (size_t)2 * ld)); wq[3] = __builtin_nontemporal_load((const f32x4*)(p + (size_t)3 * ld)); };
.Lmy_rd1_noc:
	ds_read2_b32 v[244:245], v253 offset1:1
	ds_read2_b32 v[246:247], v253 offset0:2 offset1:3
	s_cmpk_gt_i32 s46, 0x1ff
	s_cbranch_scc1 .Lmy_rd1_ldummy
	s_cmp_lt_u32 s61, 24
	s_cbranch_scc0 .Lmy_rd1_ldummy
	s_lshr_b32 s73, s61, 2
	s_lshl_b32 s73, s73, 9
	s_add_i32 s73, s73, s46
	s_mul_i32 s75, s73, 0xaaab
	s_lshr_b32 s75, s75, 22
	s_mul_i32 s76, s75, 0x60
	s_sub_i32 s76, s73, s76
	s_and_b32 s77, s61, 3
	s_add_i32 s75, s75, 32
	s_cmp_lt_u32 s76, 64
	s_cbranch_scc0 .Lmy_rd1_ldn
	s_lshr_b32 s78, s76, 3
	s_lshl_b32 s78, s78, 2
	s_add_i32 s78, s78, s77
	s_lshl_b32 s78, s78, 5
	s_lshl_b32 s79, s63, 2
	s_add_i32 s78, s78, s79
	s_lshl_b32 s78, s78, 13
	s_and_b32 s79, s76, 7
	s_lshl_b32 s79, s79, 10
	s_add_i32 s78, s78, s79
	s_lshl_b32 s79, s75, 23
	s_add_u32 s84, s66, s79
	s_addc_u32 s85, s67, 0
	s_add_u32 s84, s84, s78
	s_addc_u32 s85, s85, 0
	s_movk_i32 s80, 0x2000
	s_branch .Lmy_rd1_lgo

; DI unsigned pk4_fp8_mul64(float a, float b, float c, float d) { v2s_t r = {0, 0}; r = __builtin_amdgcn_cvt_scalef32_pk_fp8_f32(r, a, b, 0.015625f, false); r = __builtin_amdgcn_cvt_scalef32_pk_fp8_f32(r, c, d, 0.015625f, true); return __builtin_bit_cast(unsigned, r); }
; DI void attn_unit_a8(unsigned char* lds, const AttnArgs& a) {
;     ...
;     auto w_issue = [&](int j) __attribute__((always_inline)) { const float* src; unsigned char* dst; int ld, n0, k0; bool gu; w_decode(j, src, dst, ld, n0, k0, gu);
;         const float* p = src + (size_t)(k0 + 4 * wid) * ld + n0 + wn4;
;         wq[0] = __builtin_nontemporal_load((const f32x4*)p); wq[1] = __builtin_nontemporal_load((const f32x4*)(p + ld));
;         wq[2] = __builtin_nontemporal_load((const f32x4*)(p + (size_t)2 * ld)); wq[3] = __builtin_nontemporal_load((const f32x4*)(p + (size_t)3 * ld)); };
;     auto w_cvt = [&]() __attribute__((always_inline)) { unsigned char* t8 = lds + AT_WT + wn4 * WPITCH + 4 * wid;
; #pragma unroll
;         for (int j = 0; j < 4; ++j) *(unsigned*)(t8 + j * WPITCH) = pk4_fp8_mul64(wq[0][j], wq[1][j], wq[2][j], wq[3][j]); };
;     const int wcol = tid >> 1, whalf = tid & 1;
;     const unsigned wper_gu = (unsigned)((wcol >> 7) * 256 + (wcol & 96) + invperm32(wcol & 31)) * 1024u + 16u * whalf;
;     const unsigned wper_dn = (unsigned)fwd_lane16(wcol) * 1024u + 16u * whalf;
;     auto w_store = [&](int j) __attribute__((always_inline)) { const float* src; unsigned char* dst; int ld, n0, k0; bool gu; w_decode(j, src, dst, ld, n0, k0, gu);
;         const int nb = n0 >> 8; const unsigned uni = (unsigned)(gu ? (nb & 3) * 512 + (nb >> 2) * 128 : nb * 256) * 1024u + (unsigned)k0;
;         const unsigned off = (gu ? wper_gu : wper_dn) + uni;
;         const unsigned* t = (const unsigned*)(lds + AT_WT + wcol * WPITCH + 16 * whalf);
;         *(u32x4*)(dst + off) = (u32x4){t[0], t[1], t[2], t[3]}; };
.Lmy_rd1_lgo:
	global_load_dwordx4 v[236:239], v235, s[84:85] nt
	s_add_u32 s84, s84, s80
	s_addc_u32 s85, s85, 0
	global_load_dwordx4 v[240:243], v235, s[84:85] nt
	s_add_u32 s84, s84, s80
	s_addc_u32 s85, s85, 0
	s_cmpk_gt_i32 s46, 0x1ff
	s_cbranch_scc1 .Lmy_rd1_sdummy
	s_add_i32 s72, s61, -2
	s_cmp_lt_u32 s72, 24
	s_cbranch_scc0 .Lmy_rd1_sdummy
	s_lshr_b32 s73, s72, 2
	s_lshl_b32 s73, s73, 9
	s_add_i32 s73, s73, s46
	s_mul_i32 s75, s73, 0xaaab
	s_lshr_b32 s75, s75, 22
	s_mul_i32 s76, s75, 0x60
	s_sub_i32 s76, s73, s76
	s_and_b32 s77, s72, 3
	s_cmp_lt_u32 s76, 64
	s_cbranch_scc0 .Lmy_rd1_sdn
	s_lshr_b32 s78, s76, 3
	s_lshl_b32 s78, s78, 2
	s_add_i32 s78, s78, s77
	s_lshl_b32 s78, s78, 5
	s_and_b32 s79, s76, 7
	s_and_b32 s81, s79, 3
	s_lshl_b32 s81, s81, 9
	s_lshr_b32 s79, s79, 2
	s_lshl_b32 s79, s79, 7
	s_add_i32 s81, s81, s79
	s_lshl_b32 s81, s81, 10
	s_add_i32 s81, s81, s78
	s_lshl_b32 s79, s75, 21
	s_add_i32 s81, s81, s79
	s_add_u32 s82, s70, 0x9094000
	s_addc_u32 s83, s71, 0
	s_add_u32 s82, s82, s81
	s_addc_u32 s83, s83, 0
	s_waitcnt lgkmcnt(0)
	global_store_dwordx4 v254, v[244:247], s[82:83]
	s_branch .Lmy_rd1_sdone
.Lmy_rd1_sdn:
	s_sub_i32 s76, s76, 64
	s_lshr_b32 s78, s76, 2
	s_lshl_b32 s78, s78, 2
	s_add_i32 s78, s78, s77
	s_lshl_b32 s78, s78, 5
	s_and_b32 s79, s76, 3
	s_lshl_b32 s79, s79, 18
	s_add_i32 s81, s79, s78
	s_lshl_b32 s79, s75, 20
	s_add_i32 s81, s81, s79
	s_add_u32 s82, s70, 0x15094000
	s_addc_u32 s83, s71, 0
	s_add_u32 s82, s82, s81
	s_addc_u32 s83, s83, 0
	s_waitcnt lgkmcnt(0)
	global_store_dwordx4 v255, v[244:247], s[82:83]
	s_branch .Lmy_rd1_sdone

; DI f32x16 mfma8(v8i a, v8i b, f32x16 c) { return __builtin_amdgcn_mfma_scale_f32_32x32x64_f8f6f4(a, b, c, 0, 0, 0, 0, 0, 0); }
; DI void attn_unit_a8(unsigned char* lds, const AttnArgs& a) {
;     ...
;     auto w_store = [&](int j) __attribute__((always_inline)) { const float* src; unsigned char* dst; int ld, n0, k0; bool gu; w_decode(j, src, dst, ld, n0, k0, gu);
;         const int nb = n0 >> 8; const unsigned uni = (unsigned)(gu ? (nb & 3) * 512 + (nb >> 2) * 128 : nb * 256) * 1024u + (unsigned)k0;
;         const unsigned off = (gu ? wper_gu : wper_dn) + uni;
;         const unsigned* t = (const unsigned*)(lds + AT_WT + wcol * WPITCH + 16 * whalf);
;         *(u32x4*)(dst + off) = (u32x4){t[0], t[1], t[2], t[3]}; };
; DI void attn_unit_d8(unsigned char* lds, const AttnArgs& a) {
;     ...
;         lstore(s3, kreg0, vreg0); lstore(s4, kreg1, vreg1);
;         __syncthreads();
;         sb = s2;
;     }
;     o0[0] = mfma8(vY0, PaY, o0[0]); o1[0] = mfma8(vY0, PbY, o1[0]); o0[1] = mfma8(vY1, PaY, o0[1]); o1[1] = mfma8(vY1, PbY, o1[1]);
;     __builtin_amdgcn_s_setprio(0);
;     float lt0 = l0[0] + l0[1] + l0[2] + l0[3]; lt0 += __shfl_xor(lt0, 32);
;     float lt1 = l1[0] + l1[1] + l1[2] + l1[3]; lt1 += __shfl_xor(lt1, 32);
;     unsigned char* op = a.out8 + (size_t)(wid * 32 + r) * 1024 + 4 * h;
;     const float r0 = 16.0f / lt0, r1 = 16.0f * a.lam / lt1;
;     float ss = 0.f;
; #pragma unroll
;     for (int d = 0; d < 2; ++d)
; #pragma unroll
;         for (int i = 0; i < 16; ++i) { const float v = o0[d][i] * r0 - o1[d][i] * r1; o0[d][i] = v; ss += v * v; }
;     ss += __shfl_xor(ss, 32);
.Lmy_rd1_sdone:
	s_nop 0
	global_load_dwordx4 v[244:247], v235, s[84:85] nt
	s_add_u32 s84, s84, s80
	s_addc_u32 s85, s85, 0
	global_load_dwordx4 v[248:251], v235, s[84:85] nt
	v_xor_b32_e32 v252, 0x4000, v252
	v_xor_b32_e32 v253, 0x4000, v253
	s_add_i32 s61, s61, 1
	s_cmpk_lt_u32 s22, 0x42
	s_waitcnt vmcnt(6)
	ds_write_b64 v224, v[194:195]
	v_mfma_f32_32x32x64_f8f6f4 v[66:81], v[98:105], v[122:129], 0
	v_add_u32_e32 v98, s51, v218
	v_add_u32_e32 v99, 0x1400, v106
	v_add_u32_e32 v98, 0x1400, v98
	ds_write2_b32 v99, v204, v205 offset1:8
	s_waitcnt vmcnt(5)
	ds_write_b64 v107, v[196:197]
	ds_write2_b32 v98, v206, v207 offset1:8
	s_waitcnt lgkmcnt(0)
	s_barrier
	s_cbranch_scc1 .LBB0_1888
	s_lshl_b64 s[16:17], s[16:17], 10
	s_add_u32 s8, s10, s16
	s_addc_u32 s17, s11, s17
	s_add_u32 s16, s8, s47
	v_mfma_f32_32x32x64_f8f6f4 v[50:65], v[154:161], v[138:145], v[50:65]
	s_addc_u32 s17, s17, 0
	v_mfma_f32_32x32x64_f8f6f4 v[2:17], v[154:161], v[130:137], v[2:17]
	v_mfma_f32_32x32x64_f8f6f4 v[34:49], v[146:153], v[138:145], v[34:49]
	v_mfma_f32_32x32x64_f8f6f4 v[18:33], v[146:153], v[130:137], v[18:33]
	s_setprio 0
	v_add_f32_e32 v66, v188, v189
	v_add_f32_e32 v66, v186, v66
	v_add_f32_e32 v66, v187, v66
	ds_bpermute_b32 v67, v1, v66
	v_add_f32_e32 v68, v192, v193
	v_add_f32_e32 v68, v190, v68
	v_add_f32_e32 v68, v191, v68
	ds_bpermute_b32 v69, v1, v68
	s_waitcnt lgkmcnt(1)
	v_add_f32_e32 v66, v66, v67
	v_div_scale_f32 v67, s[18:19], v66, v66, s36
	v_rcp_f32_e32 v70, v67
	s_waitcnt lgkmcnt(0)
	v_add_f32_e32 v68, v68, v69
	v_lshlrev_b32_e32 v178, 2, v217
	s_add_i32 s46, s46, s60
	v_fma_f32 v69, -v67, v70, 1.0
	v_fmac_f32_e32 v70, v69, v70
	v_div_scale_f32 v69, vcc, s36, v66, s36
	v_mul_f32_e32 v71, v69, v70
	v_fma_f32 v72, -v67, v71, v69
	v_fmac_f32_e32 v71, v72, v70
	v_fma_f32 v67, -v67, v71, v69
	v_div_scale_f32 v69, s[18:19], v68, v68, v214
	v_rcp_f32_e32 v72, v69
	v_div_fmas_f32 v67, v67, v70, v71
	v_div_fixup_f32 v66, v67, v66, s36
	s_cmpk_gt_i32 s46, 0x1ff
	v_fma_f32 v67, -v69, v72, 1.0
	v_fmac_f32_e32 v72, v67, v72
	v_div_scale_f32 v67, vcc, v214, v68, v214
	v_mul_f32_e32 v70, v67, v72
	v_fma_f32 v71, -v69, v70, v67
	v_fmac_f32_e32 v70, v71, v72
	v_fma_f32 v67, -v69, v70, v67
	v_div_fmas_f32 v67, v67, v72, v70
	v_div_fixup_f32 v68, v67, v68, v214
	v_mul_f32_e32 v2, v2, v68
	v_fma_f32 v50, v50, v66, -v2
	v_mul_f32_e32 v2, v3, v68
	v_fma_f32 v51, v51, v66, -v2
	v_mul_f32_e32 v67, v51, v51
	v_mul_f32_e32 v2, v4, v68
	v_fmac_f32_e32 v67, v50, v50
	v_fma_f32 v52, v52, v66, -v2
	v_mul_f32_e32 v2, v5, v68
	v_fmac_f32_e32 v67, v52, v52
	v_fma_f32 v53, v53, v66, -v2
	v_mul_f32_e32 v2, v6, v68
	v_fmac_f32_e32 v67, v53, v53
	v_fma_f32 v54, v54, v66, -v2
	v_mul_f32_e32 v2, v7, v68
	v_fmac_f32_e32 v67, v54, v54
	v_fma_f32 v55, v55, v66, -v2
	v_mul_f32_e32 v2, v8, v68
	v_fmac_f32_e32 v67, v55, v55
	v_fma_f32 v56, v56, v66, -v2
	v_mul_f32_e32 v2, v9, v68
	v_fmac_f32_e32 v67, v56, v56
	v_fma_f32 v57, v57, v66, -v2
	v_mul_f32_e32 v2, v10, v68
	v_fmac_f32_e32 v67, v57, v57
	v_fma_f32 v58, v58, v66, -v2
	v_mul_f32_e32 v2, v11, v68
	v_fmac_f32_e32 v67, v58, v58
	v_fma_f32 v59, v59, v66, -v2
	v_mul_f32_e32 v2, v12, v68
	v_fmac_f32_e32 v67, v59, v59
	v_fma_f32 v60, v60, v66, -v2
	v_mul_f32_e32 v2, v13, v68
	v_fmac_f32_e32 v67, v60, v60
	v_fma_f32 v61, v61, v66, -v2
	v_mul_f32_e32 v14, v14, v68
	v_fmac_f32_e32 v67, v61, v61
	v_fma_f32 v62, v62, v66, -v14
	v_mul_f32_e32 v14, v15, v68
	v_fmac_f32_e32 v67, v62, v62
	v_fma_f32 v63, v63, v66, -v14
	v_mul_f32_e32 v14, v16, v68
	v_lshlrev_b32_e32 v69, 4, v217
	v_fmac_f32_e32 v67, v63, v63
	v_fma_f32 v64, v64, v66, -v14
	v_mul_f32_e32 v14, v17, v68
	global_load_dwordx4 v[2:5], v69, s[12:13] offset:480
	global_load_dwordx4 v[6:9], v69, s[12:13] offset:288
	global_load_dwordx4 v[10:13], v69, s[12:13] offset:256
	v_fmac_f32_e32 v67, v64, v64
	v_fma_f32 v65, v65, v66, -v14
	v_mul_f32_e32 v14, v18, v68
	v_fmac_f32_e32 v67, v65, v65
	v_fma_f32 v70, v34, v66, -v14
	v_mul_f32_e32 v14, v19, v68
	v_fmac_f32_e32 v67, v70, v70
	v_fma_f32 v71, v35, v66, -v14
	v_mul_f32_e32 v14, v20, v68
	v_fmac_f32_e32 v67, v71, v71
	v_fma_f32 v72, v36, v66, -v14
	v_mul_f32_e32 v14, v21, v68
	v_fmac_f32_e32 v67, v72, v72
	v_fma_f32 v73, v37, v66, -v14
	v_mul_f32_e32 v14, v22, v68
	v_fmac_f32_e32 v67, v73, v73
	v_fma_f32 v74, v38, v66, -v14
	v_mul_f32_e32 v14, v23, v68
	v_fmac_f32_e32 v67, v74, v74
	v_fma_f32 v75, v39, v66, -v14
	v_fmac_f32_e32 v67, v75, v75
	v_pk_mul_f32 v[14:15], v[24:25], v[68:69] op_sel_hi:[1,0]
	v_pk_mul_f32 v[22:23], v[32:33], v[68:69] op_sel_hi:[1,0]
	v_pk_fma_f32 v[34:35], v[40:41], v[66:67], v[14:15] op_sel_hi:[1,0,1] neg_lo:[0,0,1] neg_hi:[0,0,1]
	s_nop 0
	v_pk_mul_f32 v[14:15], v[34:35], v[34:35]
	s_nop 0
	v_add_f32_e32 v14, v14, v67
	v_add_f32_e32 v20, v15, v14
	v_pk_mul_f32 v[14:15], v[26:27], v[68:69] op_sel_hi:[1,0]
	s_nop 0
	v_pk_fma_f32 v[36:37], v[42:43], v[66:67], v[14:15] op_sel_hi:[1,0,1] neg_lo:[0,0,1] neg_hi:[0,0,1]
	global_load_dwordx4 v[14:17], v69, s[12:13] offset:320
	v_pk_mul_f32 v[18:19], v[36:37], v[36:37]
	v_pk_fma_f32 v[42:43], v[48:49], v[66:67], v[22:23] op_sel_hi:[1,0,1] neg_lo:[0,0,1] neg_hi:[0,0,1]
	v_add_f32_e32 v18, v18, v20
	v_add_f32_e32 v20, v19, v18
	v_pk_mul_f32 v[18:19], v[28:29], v[68:69] op_sel_hi:[1,0]
	v_pk_mul_f32 v[22:23], v[42:43], v[42:43]
	v_pk_fma_f32 v[38:39], v[44:45], v[66:67], v[18:19] op_sel_hi:[1,0,1] neg_lo:[0,0,1] neg_hi:[0,0,1]
	s_nop 0
	v_pk_mul_f32 v[18:19], v[38:39], v[38:39]
	s_nop 0
	v_add_f32_e32 v18, v18, v20
	v_add_f32_e32 v20, v19, v18
	v_pk_mul_f32 v[18:19], v[30:31], v[68:69] op_sel_hi:[1,0]
	s_nop 0
	v_pk_fma_f32 v[40:41], v[46:47], v[66:67], v[18:19] op_sel_hi:[1,0,1] neg_lo:[0,0,1] neg_hi:[0,0,1]
	s_nop 0
	v_pk_mul_f32 v[18:19], v[40:41], v[40:41]
	s_nop 0
	v_add_f32_e32 v18, v18, v20
	v_add_f32_e32 v24, v19, v18
	v_add_f32_e32 v22, v22, v24
	v_add_f32_e32 v26, v23, v22
	ds_bpermute_b32 v27, v1, v26
	global_load_dwordx4 v[18:21], v69, s[12:13] offset:352
	global_load_dwordx4 v[22:25], v69, s[12:13] offset:448
	s_waitcnt lgkmcnt(0)
; DI unsigned pk4_fp8(float a, float b, float c, float d) { int r = 0; r = __builtin_amdgcn_cvt_pk_fp8_f32(a, b, r, false); r = __builtin_amdgcn_cvt_pk_fp8_f32(c, d, r, true); return (unsigned)r; }
; DI float clamp448(float x) { return __builtin_amdgcn_fmed3f(x, -448.0f, 448.0f); }
; DI void attn_unit_d8(unsigned char* lds, const AttnArgs& a) {
;     ...
;     const float rinv = rsqrtf(ss * (1.0f / 64.0f) + EPS) * a.oscale * CAT_SCALE;
;     f32x4 ggv[2][4];
; #pragma unroll
;     for (int d = 0; d < 2; ++d)
; #pragma unroll
;         for (int g = 0; g < 4; ++g) ggv[d][g] = *(const f32x4*)(a.subg + 32 * d + 8 * g + 4 * h);
;     asm volatile("" : "+v"(ggv[0][0]), "+v"(ggv[1][3]));
; #pragma unroll
;     for (int d = 0; d < 2; ++d)
; #pragma unroll
;         for (int g = 0; g < 4; ++g) { const f32x4 gg = ggv[d][g];
;             *(unsigned*)(op + 32 * d + 8 * g) = pk4_fp8(clamp448(o0[d][4 * g] * rinv * gg[0]), clamp448(o0[d][4 * g + 1] * rinv * gg[1]), clamp448(o0[d][4 * g + 2] * rinv * gg[2]), clamp448(o0[d][4 * g + 3] * rinv * gg[3])); }
	v_add_f32_e32 v26, v26, v27
	v_fmamk_f32 v26, v26, 0x3c800000, v215
	v_mul_f32_e32 v27, 0x4b800000, v26
	v_cmp_gt_f32_e32 vcc, s41, v26
	s_nop 1
	v_cndmask_b32_e32 v30, v26, v27, vcc
	global_load_dwordx4 v[26:29], v69, s[12:13] offset:384
	v_rsq_f32_e32 v32, v30
	v_lshlrev_b64 v[30:31], 10, v[180:181]
	v_lshl_add_u64 v[44:45], s[16:17], 0, v[30:31]
	v_lshl_add_u64 v[44:45], v[44:45], 0, v[178:179]
	v_mul_f32_e32 v30, 0x45800000, v32
	v_cndmask_b32_e32 v30, v32, v30, vcc
	v_mul_f32_e32 v48, v213, v30
	global_load_dwordx4 v[30:33], v69, s[12:13] offset:416
	v_mul_f32_e32 v48, 0x41800000, v48
	s_waitcnt vmcnt(5)
	v_mul_f32_e32 v49, v50, v48
	v_mul_f32_e32 v10, v10, v49
	v_mul_f32_e32 v49, v51, v48
	v_mul_f32_e32 v11, v11, v49
	v_mul_f32_e32 v49, v52, v48
	v_med3_f32 v10, v10, s42, v216
	v_med3_f32 v11, v11, s42, v216
	v_mul_f32_e32 v12, v12, v49
	s_nop 0
	v_cvt_pk_fp8_f32 v49, v10, v11
	v_mul_f32_e32 v10, v53, v48
	v_mul_f32_e32 v10, v13, v10
	v_med3_f32 v12, v12, s42, v216
	v_med3_f32 v10, v10, s42, v216
	v_cvt_pk_fp8_f32 v49, v12, v10 op_sel:[0,0,1]
	v_mul_f32_e32 v10, v54, v48
	v_mul_f32_e32 v6, v6, v10
	v_mul_f32_e32 v10, v55, v48
	v_mul_f32_e32 v7, v7, v10
	v_mul_f32_e32 v10, v56, v48
	v_med3_f32 v6, v6, s42, v216
	v_med3_f32 v7, v7, s42, v216
	v_mul_f32_e32 v8, v8, v10
	s_nop 0
	v_cvt_pk_fp8_f32 v10, v6, v7
	v_mul_f32_e32 v6, v57, v48
	v_mul_f32_e32 v6, v9, v6
	v_med3_f32 v8, v8, s42, v216
	v_med3_f32 v6, v6, s42, v216
	v_cvt_pk_fp8_f32 v10, v8, v6 op_sel:[0,0,1]
	v_add_co_u32_e32 v6, vcc, s43, v44
	v_lshl_add_u64 v[46:47], v[44:45], 0, s[14:15]
	s_nop 0
	v_addc_co_u32_e32 v7, vcc, 0, v45, vcc
	global_store_dword v[6:7], v49, off offset:768
	global_store_dword v[46:47], v10, off offset:8
	v_mul_f32_e32 v6, v58, v48
	v_mul_f32_e32 v7, v59, v48
	s_waitcnt vmcnt(6)
	v_mul_f32_e32 v6, v14, v6
	v_mul_f32_e32 v7, v15, v7
	v_med3_f32 v6, v6, s42, v216
	v_med3_f32 v7, v7, s42, v216
	s_nop 0
	v_cvt_pk_fp8_f32 v9, v6, v7
	v_mul_f32_e32 v8, v60, v48
	v_mul_f32_e32 v6, v61, v48
	v_mul_f32_e32 v8, v16, v8
	v_mul_f32_e32 v6, v17, v6
	v_med3_f32 v8, v8, s42, v216
	v_med3_f32 v6, v6, s42, v216
	v_cvt_pk_fp8_f32 v9, v8, v6 op_sel:[0,0,1]
	v_mul_f32_e32 v6, v62, v48
	v_mul_f32_e32 v7, v63, v48
	s_nop 0
	v_mul_f32_e32 v8, v64, v48
	s_nop 0
	s_waitcnt vmcnt(5)
	v_mul_f32_e32 v6, v18, v6
	v_mul_f32_e32 v7, v19, v7
	v_med3_f32 v6, v6, s42, v216
	v_med3_f32 v7, v7, s42, v216
	v_cvt_pk_fp8_f32 v10, v6, v7
	v_mul_f32_e32 v6, v65, v48
	v_mul_f32_e32 v8, v20, v8
	v_mul_f32_e32 v6, v21, v6
	v_med3_f32 v8, v8, s42, v216
	v_med3_f32 v6, v6, s42, v216
	v_cvt_pk_fp8_f32 v10, v8, v6 op_sel:[0,0,1]
	v_mul_f32_e32 v6, v70, v48
	v_mul_f32_e32 v7, v71, v48
	s_waitcnt vmcnt(3)
	v_mul_f32_e32 v6, v26, v6
	v_mul_f32_e32 v7, v27, v7
	v_med3_f32 v6, v6, s42, v216
	v_med3_f32 v7, v7, s42, v216
	v_cvt_pk_fp8_f32 v11, v6, v7
	v_mul_f32_e32 v8, v72, v48
	v_mul_f32_e32 v6, v73, v48
	v_mul_f32_e32 v8, v28, v8
	v_mul_f32_e32 v6, v29, v6
	v_med3_f32 v8, v8, s42, v216
	v_med3_f32 v6, v6, s42, v216
	v_cvt_pk_fp8_f32 v11, v8, v6 op_sel:[0,0,1]
	v_mul_f32_e32 v6, v74, v48
	v_mul_f32_e32 v7, v75, v48
	s_waitcnt vmcnt(2)
	v_mul_f32_e32 v6, v30, v6
	v_mul_f32_e32 v7, v31, v7
	v_med3_f32 v6, v6, s42, v216
	v_med3_f32 v7, v7, s42, v216
	s_nop 0
	v_cvt_pk_fp8_f32 v12, v6, v7
	v_mul_f32_e32 v8, v34, v48
	v_mul_f32_e32 v6, v35, v48
	v_mul_f32_e32 v8, v32, v8
	v_mul_f32_e32 v6, v33, v6
	v_med3_f32 v8, v8, s42, v216
	v_med3_f32 v6, v6, s42, v216
	v_cvt_pk_fp8_f32 v12, v8, v6 op_sel:[0,0,1]
	v_mul_f32_e32 v6, v36, v48
	v_mul_f32_e32 v7, v37, v48
	v_mul_f32_e32 v6, v22, v6
	v_mul_f32_e32 v7, v23, v7
	global_store_dword v[46:47], v9, off offset:16
	global_store_dword v[46:47], v10, off offset:24
	global_store_dword v[46:47], v11, off offset:32
	global_store_dword v[46:47], v12, off offset:40
	v_med3_f32 v6, v6, s42, v216
	v_med3_f32 v7, v7, s42, v216
	s_nop 0
	v_cvt_pk_fp8_f32 v9, v6, v7
	v_mul_f32_e32 v8, v38, v48
	v_mul_f32_e32 v6, v39, v48
	v_mul_f32_e32 v8, v24, v8
	v_mul_f32_e32 v6, v25, v6
	v_med3_f32 v8, v8, s42, v216
	v_med3_f32 v6, v6, s42, v216
	v_cvt_pk_fp8_f32 v9, v8, v6 op_sel:[0,0,1]
	v_mul_f32_e32 v6, v40, v48
	v_mul_f32_e32 v2, v2, v6
	v_mul_f32_e32 v6, v41, v48
	v_mul_f32_e32 v3, v3, v6
	v_mul_f32_e32 v6, v42, v48
	v_med3_f32 v2, v2, s42, v216
	v_med3_f32 v3, v3, s42, v216
	v_mul_f32_e32 v4, v4, v6
	s_nop 0
	v_cvt_pk_fp8_f32 v6, v2, v3
	v_mul_f32_e32 v2, v43, v48
	v_mul_f32_e32 v2, v5, v2
	v_med3_f32 v4, v4, s42, v216
	v_med3_f32 v2, v2, s42, v216
	v_cvt_pk_fp8_f32 v6, v4, v2 op_sel:[0,0,1]
	global_store_dword v[46:47], v9, off offset:48
	global_store_dword v[46:47], v6, off offset:56
	s_cbranch_scc0 .LBB0_1885

; DI void attn_unit_a8(unsigned char* lds, const AttnArgs& a) {
;     ...
;     { const bf16_t* qp = a.q + (size_t)(wid * 32 + r) * 256 + 32 * h;
;       const u32x4 q0 = *(const u32x4*)qp, q1 = *(const u32x4*)(qp + 8), q2 = *(const u32x4*)(qp + 16), q3 = *(const u32x4*)(qp + 24);
;       const u32x2 c0 = bf8_to_fp8(q0), c1 = bf8_to_fp8(q1), c2 = bf8_to_fp8(q2), c3 = bf8_to_fp8(q3);
;       qf8 = (v8i){(int)c0.x, (int)c0.y, (int)c1.x, (int)c1.y, (int)c2.x, (int)c2.y, (int)c3.x, (int)c3.y}; }
;     ...
;     const bool wrider = a.wl >= 0;
;     if (wrider) w_issue(0);
.LBB0_1914:
	s_ashr_i32 s75, s76, 6
	s_lshl_b32 s78, s76, 8
	s_lshl_b32 s10, s75, 12
	s_and_b32 s8, s78, 0xf00
	s_or_b32 s40, s10, s8
	s_ashr_i32 s41, s40, 31
	s_bfe_u32 s20, s76, 0x20004
	s_lshl_b64 s[12:13], s[40:41], 9
	s_add_u32 s8, s28, s12
	s_addc_u32 s11, s29, s13
	s_lshl_b32 s12, s20, 7
	v_mov_b32_e32 v167, v0
	s_add_u32 s12, s8, s12
	s_addc_u32 s13, s11, 0
	v_readfirstlane_b32 s8, v167
	v_and_b32_e32 v21, 31, v167
	s_ashr_i32 s79, s8, 6
	v_lshl_or_b32 v128, s79, 5, v21
	v_ashrrev_i32_e32 v129, 31, v128
	v_lshlrev_b64 v[2:3], 9, v[128:129]
	v_and_b32_e32 v22, 32, v167
	v_lshl_add_u64 v[2:3], s[12:13], 0, v[2:3]
	v_lshlrev_b32_e32 v106, 1, v22
	v_lshl_add_u64 v[14:15], v[2:3], 0, v[106:107]
	global_load_dwordx4 v[2:5], v[14:15], off offset:48
	global_load_dwordx4 v[6:9], v[14:15], off offset:32
	global_load_dwordx4 v[10:13], v[14:15], off offset:16
	s_nop 0
	global_load_dwordx4 v[14:17], v[14:15], off
	v_lshlrev_b32_e32 v18, 2, v167
	s_cmp_gt_i32 s76, 0x10000
	s_cselect_b64 s[50:51], -1, 0
	s_cmp_lt_i32 s76, 0x10000
	v_and_b32_e32 v20, 0xfc, v18
	s_cbranch_scc1 .LBB0_1920
	s_mul_i32 s8, s76, 0xaaab
	s_lshr_b32 s8, s8, 22
	s_mul_i32 s11, s8, 0xffffffa0
	s_add_i32 s11, s11, s76
	s_mov_b64 s[16:17], s[0:1]
	s_cmp_gt_i32 s11, 63
	s_mov_b64 s[18:19], -1
	s_cbranch_scc0 .LBB0_1917
	s_load_dwordx2 s[12:13], s[16:17], 0xc0
	s_lshl_b32 s14, s8, 22
	s_mov_b64 s[18:19], 0
	s_waitcnt lgkmcnt(0)
	s_add_u32 s12, s12, s14
	s_addc_u32 s13, s13, 0
	s_add_u32 s12, s12, 0x8000000
	s_addc_u32 s13, s13, 0
	s_and_b32 s15, s11, 0x7ffffffc
	s_and_b32 s14, s78, 0x300
	s_sub_i32 s15, s15, 64

; __global__ void __launch_bounds__(512, 2) mega(Params Pdummy) {
	.amdhsa_kernel _Z4mega6Params
		.amdhsa_group_segment_fixed_size 0
		.amdhsa_private_segment_fixed_size 0
		.amdhsa_kernarg_size 488
		.amdhsa_user_sgpr_count 2
		.amdhsa_user_sgpr_dispatch_ptr 0
		.amdhsa_user_sgpr_queue_ptr 0
		.amdhsa_user_sgpr_kernarg_segment_ptr 1
		.amdhsa_user_sgpr_dispatch_id 0
		.amdhsa_user_sgpr_kernarg_preload_length 0
		.amdhsa_user_sgpr_kernarg_preload_offset 0
		.amdhsa_user_sgpr_private_segment_size 0
		.amdhsa_uses_dynamic_stack 0
		.amdhsa_enable_private_segment 0
		.amdhsa_system_sgpr_workgroup_id_x 1
		.amdhsa_system_sgpr_workgroup_id_y 0
		.amdhsa_system_sgpr_workgroup_id_z 0
		.amdhsa_system_sgpr_workgroup_info 0
		.amdhsa_system_vgpr_workitem_id 0
		.amdhsa_next_free_vgpr 256
		.amdhsa_next_free_sgpr 98
		.amdhsa_accum_offset 256
		.amdhsa_reserve_vcc 1
		.amdhsa_float_round_mode_32 0
		.amdhsa_float_round_mode_16_64 0
		.amdhsa_float_denorm_mode_32 3
		.amdhsa_float_denorm_mode_16_64 3
		.amdhsa_dx10_clamp 1
		.amdhsa_ieee_mode 1
		.amdhsa_fp16_overflow 0
		.amdhsa_tg_split 0
		.amdhsa_exception_fp_ieee_invalid_op 0
		.amdhsa_exception_fp_denorm_src 0
		.amdhsa_exception_fp_ieee_div_zero 0
		.amdhsa_exception_fp_ieee_overflow 0
		.amdhsa_exception_fp_ieee_underflow 0
		.amdhsa_exception_fp_ieee_inexact 0
		.amdhsa_exception_int_div_zero 0
	.end_amdhsa_kernel

; __global__ void __launch_bounds__(512, 2) mega(Params Pdummy) {
amdhsa.kernels:
  - .agpr_count:     0
    .args:
      - .offset:         0
        .size:           232
        .value_kind:     by_value
      - .offset:         232
        .size:           4
        .value_kind:     hidden_block_count_x
      - .offset:         236
        .size:           4
        .value_kind:     hidden_block_count_y
      - .offset:         240
        .size:           4
        .value_kind:     hidden_block_count_z
      - .offset:         244
        .size:           2
        .value_kind:     hidden_group_size_x
      - .offset:         246
        .size:           2
        .value_kind:     hidden_group_size_y
      - .offset:         248
        .size:           2
        .value_kind:     hidden_group_size_z
      - .offset:         250
        .size:           2
        .value_kind:     hidden_remainder_x
      - .offset:         252
        .size:           2
        .value_kind:     hidden_remainder_y
      - .offset:         254
        .size:           2
        .value_kind:     hidden_remainder_z
      - .offset:         272
        .size:           8
        .value_kind:     hidden_global_offset_x
      - .offset:         280
        .size:           8
        .value_kind:     hidden_global_offset_y
      - .offset:         288
        .size:           8
        .value_kind:     hidden_global_offset_z
      - .offset:         296
        .size:           2
        .value_kind:     hidden_grid_dims
      - .offset:         352
        .size:           4
        .value_kind:     hidden_dynamic_lds_size
    .group_segment_fixed_size: 0
    .kernarg_segment_align: 8
    .kernarg_segment_size: 488
    .language:       OpenCL C
    .language_version:
      - 2
      - 0
    .max_flat_workgroup_size: 512
    .name:           _Z4mega6Params
    .private_segment_fixed_size: 0
    .sgpr_count:     104
    .sgpr_spill_count: 17
    .symbol:         _Z4mega6Params.kd
    .uniform_work_group_size: 1
    .uses_dynamic_stack: false
    .vgpr_count:     256
    .vgpr_spill_count: 0
    .wavefront_size: 64
